# GEMM K-loops: the four VGPR-addressed LDS-DMA staging loads per iteration now use scalar base arithmetic (8 fewer 64-bit vector adds per iteration)
# speedup vs baseline: 1.0026x; 1.0026x over previous
; #define PG8_STAGE(bufoff, gbase, voff) do { _Pragma("unroll") for (int _i = 0; _i < 2; ++_i) { unsigned _vo = (voff)[_i]; asm volatile("" : "+v"(_vo));     \
;         __builtin_amdgcn_global_load_lds((const unsigned*)((const char*)(gbase) + _vo), (PG8_LAS unsigned*)(lds + (bufoff) + ldsw + _i * 8192), 16, 0, 0); } } while (0)
; #define PG8_LDA(dst, b, h) do { _Pragma("unroll") for (int m = 0; m < 4; ++m) _Pragma("unroll") for (int k = 0; k < 2; ++k) dst[m][k] = *(const PG8_LAS bf16x8*)(lds + PG8_SA(b, h) + aoff + m * 2048 + k * 1024); } while (0)
; #define PG8_LDB(dst, b, h) do { _Pragma("unroll") for (int n = 0; n < 2; ++n) _Pragma("unroll") for (int k = 0; k < 2; ++k) dst[n][k] = *(const PG8_LAS bf16x8*)(lds + PG8_SB(b, h) + boff + n * 2048 + k * 1024); } while (0)
; #define PG8_WAIT_V(n) asm volatile("s_waitcnt vmcnt(" #n ")" ::: "memory")
; #define PG8_WAIT_L(n) asm volatile("s_waitcnt lgkmcnt(" #n ")" ::: "memory")
; #define PG8_BAR __builtin_amdgcn_s_barrier()
; #define PG8_SCHED __builtin_amdgcn_sched_barrier(0)
; template <class Epi, class Sched, bool ALIGN_EPI = false, bool SP2 = false, bool FP8 = false>
; __device__ __forceinline__ void gemm_phase(PG8_LAS unsigned char* lds, const Gemm g, const Sched& S, const Epi& E, const int wave_) {
;     ...
;         for (int t = 0; t < ntc; t += 2) {
;             const bool last = (t == ntc - 2);
;             const char* a1 = cA + (size_t)(t + 1) * kstep;
;             const char* a2 = last ? nA : cA + (size_t)(t + 2) * kstep; const char* b2 = last ? nB : cB + (size_t)(t + 2) * kstep;
;             const char* a3 = a2 + kstep; const char* b3 = b2 + kstep;
;             if (last && has_next) S.a_ready(nxt);
;             if constexpr (SP2) {
;             PG8_LDB(B0, 0, 0); PG8_LDB(B1, 0, 1); PG8_SCHED; PG8_LDA(At, 0, 0); PG8_STAGE(PG8_SA(1, 1), a1 + hstep, voffA);
;             PG8_WAIT_V(8); PG8_WAIT_L(0); PG8_BAR; PG8_MMA(0, 0, At, B0); PG8_MMA(0, 1, At, B1); PG8_BAR; PG8_SCHED;
;             PG8_LDA(At, 0, 1); PG8_STAGE(PG8_SB(0, 0), b2, voffB); PG8_STAGE(PG8_SB(0, 1), b2 + hstep, voffB); PG8_STAGE(PG8_SA(0, 0), a2, voffA);
;             PG8_WAIT_V(8); PG8_WAIT_L(0); PG8_BAR; PG8_MMA(1, 0, At, B0); PG8_MMA(1, 1, At, B1); PG8_BAR; PG8_SCHED;
.LBB0_169:
	s_add_u32 s28, s26, 0xfff80080
	s_addc_u32 s29, s27, -1
	s_add_i32 s62, 0, 0x10000
	s_cmp_eq_u32 s47, 28
	s_cselect_b32 s29, s18, s29
	s_cselect_b32 s28, s19, s28
	v_add_u32_e32 v0, s62, v148
	s_cselect_b32 s35, s17, s46
	s_cselect_b32 s34, s21, s45
	s_add_i32 s64, 0, 0x14000
	ds_read_b128 v[114:117], v0
	ds_read_b128 v[118:121], v0 offset:1024
	ds_read_b128 v[138:141], v0 offset:2048
	ds_read_b128 v[150:153], v0 offset:3072
	v_add_u32_e32 v0, s64, v148
	ds_read_b128 v[154:157], v0
	ds_read_b128 v[158:161], v0 offset:1024
	ds_read_b128 v[170:173], v0 offset:2048
	ds_read_b128 v[174:177], v0 offset:3072
	v_mov_b32_e32 v0, v144
	ds_read_b128 v[178:181], v149
	ds_read_b128 v[182:185], v149 offset:1024
	ds_read_b128 v[186:189], v149 offset:2048
	ds_read_b128 v[190:193], v149 offset:3072
	ds_read_b128 v[208:211], v149 offset:4096
	ds_read_b128 v[212:215], v149 offset:5120
	ds_read_b128 v[216:219], v149 offset:6144
	ds_read_b128 v[220:223], v149 offset:7168
	s_add_i32 m0, s54, 0xc000
	s_nop 0
	global_load_lds_dwordx4 v0, s[26:27]
	v_mov_b32_e32 v0, v146
	s_add_i32 m0, s54, 0xe000
	s_nop 0
	global_load_lds_dwordx4 v0, s[26:27]
	s_waitcnt vmcnt(8)
	s_waitcnt lgkmcnt(0)
	s_barrier
	s_setprio 1
	s_waitcnt lgkmcnt(0)
	v_mfma_f32_16x16x32_bf16 v[130:133], v[114:117], v[178:181], v[130:133]
	v_mfma_f32_16x16x32_bf16 v[134:137], v[138:141], v[178:181], v[134:137]
	v_mfma_f32_16x16x32_bf16 v[122:125], v[114:117], v[186:189], v[122:125]
	v_mfma_f32_16x16x32_bf16 v[126:129], v[138:141], v[186:189], v[126:129]
	v_mfma_f32_16x16x32_bf16 v[106:109], v[114:117], v[208:211], v[106:109]
	v_mfma_f32_16x16x32_bf16 v[110:113], v[138:141], v[208:211], v[110:113]
	v_mfma_f32_16x16x32_bf16 v[98:101], v[114:117], v[216:219], v[98:101]
	v_mfma_f32_16x16x32_bf16 v[102:105], v[138:141], v[216:219], v[102:105]
	v_mfma_f32_16x16x32_bf16 v[130:133], v[118:121], v[182:185], v[130:133]
	v_mfma_f32_16x16x32_bf16 v[134:137], v[150:153], v[182:185], v[134:137]
	v_mfma_f32_16x16x32_bf16 v[122:125], v[118:121], v[190:193], v[122:125]
	v_mfma_f32_16x16x32_bf16 v[126:129], v[150:153], v[190:193], v[126:129]
	v_mfma_f32_16x16x32_bf16 v[106:109], v[118:121], v[212:215], v[106:109]
	v_mfma_f32_16x16x32_bf16 v[110:113], v[150:153], v[212:215], v[110:113]
	v_mfma_f32_16x16x32_bf16 v[98:101], v[118:121], v[220:223], v[98:101]
	v_mfma_f32_16x16x32_bf16 v[102:105], v[150:153], v[220:223], v[102:105]
	s_setprio 0
	s_setprio 1
	v_mfma_f32_16x16x32_bf16 v[62:65], v[154:157], v[178:181], v[62:65]
	v_mfma_f32_16x16x32_bf16 v[30:33], v[170:173], v[178:181], v[30:33]
	v_mfma_f32_16x16x32_bf16 v[58:61], v[154:157], v[186:189], v[58:61]
	v_mfma_f32_16x16x32_bf16 v[26:29], v[170:173], v[186:189], v[26:29]
	v_mfma_f32_16x16x32_bf16 v[54:57], v[154:157], v[208:211], v[54:57]
	v_mfma_f32_16x16x32_bf16 v[22:25], v[170:173], v[208:211], v[22:25]
	v_mfma_f32_16x16x32_bf16 v[50:53], v[154:157], v[216:219], v[50:53]
	v_mfma_f32_16x16x32_bf16 v[18:21], v[170:173], v[216:219], v[18:21]
	v_mfma_f32_16x16x32_bf16 v[62:65], v[158:161], v[182:185], v[62:65]
	v_mfma_f32_16x16x32_bf16 v[30:33], v[174:177], v[182:185], v[30:33]
	v_mfma_f32_16x16x32_bf16 v[58:61], v[158:161], v[190:193], v[58:61]
	v_mfma_f32_16x16x32_bf16 v[26:29], v[174:177], v[190:193], v[26:29]
	v_mfma_f32_16x16x32_bf16 v[54:57], v[158:161], v[212:215], v[54:57]
	v_mfma_f32_16x16x32_bf16 v[22:25], v[174:177], v[212:215], v[22:25]
	v_mfma_f32_16x16x32_bf16 v[50:53], v[158:161], v[220:223], v[50:53]
	v_mfma_f32_16x16x32_bf16 v[18:21], v[174:177], v[220:223], v[18:21]
	s_setprio 0
	s_barrier
	v_mov_b32_e32 v0, v145
	s_add_i32 s62, s62, s33
	ds_read_b128 v[178:181], v149 offset:16384
	ds_read_b128 v[182:185], v149 offset:17408
	ds_read_b128 v[186:189], v149 offset:18432
	ds_read_b128 v[190:193], v149 offset:19456
	ds_read_b128 v[208:211], v149 offset:20480
	ds_read_b128 v[212:215], v149 offset:21504
	ds_read_b128 v[216:219], v149 offset:22528
	ds_read_b128 v[220:223], v149 offset:23552
	s_mov_b32 m0, s62
	s_nop 0
	global_load_lds_dwordx4 v0, s[34:35]
	v_mov_b32_e32 v0, v147
	s_add_i32 m0, s62, 0x2000
	s_add_u32 s62, s34, 0x80000
	global_load_lds_dwordx4 v0, s[34:35]
	s_addc_u32 s63, s35, 0
	v_mov_b32_e32 v0, v145
	s_add_i32 s64, s64, s33
	s_mov_b32 m0, s64
	s_nop 0
	global_load_lds_dwordx4 v0, s[62:63]
	v_mov_b32_e32 v0, v147
	s_add_i32 m0, s64, 0x2000
	s_nop 0
	global_load_lds_dwordx4 v0, s[62:63]
	v_mov_b32_e32 v0, v144
	s_mov_b32 m0, s54
	s_nop 0
	global_load_lds_dwordx4 v0, s[28:29]
	v_mov_b32_e32 v0, v146
	s_mov_b32 m0, s55
	s_nop 0
	global_load_lds_dwordx4 v0, s[28:29]
	s_waitcnt vmcnt(8)
	s_waitcnt lgkmcnt(0)
	s_barrier
; #define PG8_STAGE(bufoff, gbase, voff) do { _Pragma("unroll") for (int _i = 0; _i < 2; ++_i) { unsigned _vo = (voff)[_i]; asm volatile("" : "+v"(_vo));     \
;         __builtin_amdgcn_global_load_lds((const unsigned*)((const char*)(gbase) + _vo), (PG8_LAS unsigned*)(lds + (bufoff) + ldsw + _i * 8192), 16, 0, 0); } } while (0)
; #define PG8_LDA(dst, b, h) do { _Pragma("unroll") for (int m = 0; m < 4; ++m) _Pragma("unroll") for (int k = 0; k < 2; ++k) dst[m][k] = *(const PG8_LAS bf16x8*)(lds + PG8_SA(b, h) + aoff + m * 2048 + k * 1024); } while (0)
; #define PG8_LDB(dst, b, h) do { _Pragma("unroll") for (int n = 0; n < 2; ++n) _Pragma("unroll") for (int k = 0; k < 2; ++k) dst[n][k] = *(const PG8_LAS bf16x8*)(lds + PG8_SB(b, h) + boff + n * 2048 + k * 1024); } while (0)
; #define PG8_WAIT_V(n) asm volatile("s_waitcnt vmcnt(" #n ")" ::: "memory")
; #define PG8_WAIT_L(n) asm volatile("s_waitcnt lgkmcnt(" #n ")" ::: "memory")
; #define PG8_BAR __builtin_amdgcn_s_barrier()
; #define PG8_SCHED __builtin_amdgcn_sched_barrier(0)
; template <class Epi, class Sched, bool ALIGN_EPI = false, bool SP2 = false, bool FP8 = false>
; __device__ __forceinline__ void gemm_phase(PG8_LAS unsigned char* lds, const Gemm g, const Sched& S, const Epi& E, const int wave_) {
;     ...
;             PG8_WAIT_V(8); PG8_WAIT_L(0); PG8_BAR; PG8_MMA(1, 0, At, B0); PG8_MMA(1, 1, At, B1); PG8_BAR; PG8_SCHED;
;             PG8_LDB(B0, 1, 0); PG8_LDB(B1, 1, 1); PG8_SCHED; PG8_LDA(At, 1, 0); PG8_STAGE(PG8_SA(0, 1), a2 + hstep, voffA);
;             PG8_WAIT_V(8); PG8_WAIT_L(0); PG8_BAR; PG8_MMA(0, 0, At, B0); PG8_MMA(0, 1, At, B1); PG8_BAR; PG8_SCHED;
	s_setprio 1
	s_waitcnt lgkmcnt(0)
	v_mfma_f32_16x16x32_bf16 v[90:93], v[114:117], v[178:181], v[90:93]
	v_mfma_f32_16x16x32_bf16 v[94:97], v[138:141], v[178:181], v[94:97]
	v_mfma_f32_16x16x32_bf16 v[82:85], v[114:117], v[186:189], v[82:85]
	v_mfma_f32_16x16x32_bf16 v[86:89], v[138:141], v[186:189], v[86:89]
	v_mfma_f32_16x16x32_bf16 v[74:77], v[114:117], v[208:211], v[74:77]
	v_mfma_f32_16x16x32_bf16 v[78:81], v[138:141], v[208:211], v[78:81]
	v_mfma_f32_16x16x32_bf16 v[66:69], v[114:117], v[216:219], v[66:69]
	v_mfma_f32_16x16x32_bf16 v[70:73], v[138:141], v[216:219], v[70:73]
	v_mfma_f32_16x16x32_bf16 v[90:93], v[118:121], v[182:185], v[90:93]
	v_mfma_f32_16x16x32_bf16 v[94:97], v[150:153], v[182:185], v[94:97]
	v_mfma_f32_16x16x32_bf16 v[82:85], v[118:121], v[190:193], v[82:85]
	v_mfma_f32_16x16x32_bf16 v[86:89], v[150:153], v[190:193], v[86:89]
	v_mfma_f32_16x16x32_bf16 v[74:77], v[118:121], v[212:215], v[74:77]
	v_mfma_f32_16x16x32_bf16 v[78:81], v[150:153], v[212:215], v[78:81]
	v_mfma_f32_16x16x32_bf16 v[66:69], v[118:121], v[220:223], v[66:69]
	v_mfma_f32_16x16x32_bf16 v[70:73], v[150:153], v[220:223], v[70:73]
	s_setprio 0
	s_setprio 1
	v_mfma_f32_16x16x32_bf16 v[46:49], v[154:157], v[178:181], v[46:49]
	v_mfma_f32_16x16x32_bf16 v[14:17], v[170:173], v[178:181], v[14:17]
	v_mfma_f32_16x16x32_bf16 v[42:45], v[154:157], v[186:189], v[42:45]
	v_mfma_f32_16x16x32_bf16 v[10:13], v[170:173], v[186:189], v[10:13]
	v_mfma_f32_16x16x32_bf16 v[38:41], v[154:157], v[208:211], v[38:41]
	v_mfma_f32_16x16x32_bf16 v[6:9], v[170:173], v[208:211], v[6:9]
	v_mfma_f32_16x16x32_bf16 v[34:37], v[154:157], v[216:219], v[34:37]
	v_mfma_f32_16x16x32_bf16 v[2:5], v[170:173], v[216:219], v[2:5]
	v_mfma_f32_16x16x32_bf16 v[46:49], v[158:161], v[182:185], v[46:49]
	v_mfma_f32_16x16x32_bf16 v[14:17], v[174:177], v[182:185], v[14:17]
	v_mfma_f32_16x16x32_bf16 v[42:45], v[158:161], v[190:193], v[42:45]
	v_mfma_f32_16x16x32_bf16 v[10:13], v[174:177], v[190:193], v[10:13]
	v_mfma_f32_16x16x32_bf16 v[38:41], v[158:161], v[212:215], v[38:41]
	v_mfma_f32_16x16x32_bf16 v[6:9], v[174:177], v[212:215], v[6:9]
	v_mfma_f32_16x16x32_bf16 v[34:37], v[158:161], v[220:223], v[34:37]
	v_mfma_f32_16x16x32_bf16 v[2:5], v[174:177], v[220:223], v[2:5]
	s_setprio 0
	s_barrier
	s_add_i32 s64, 0, 0x18000
	v_add_u32_e32 v0, s64, v148
	s_add_i32 s65, 0, 0x1c000
	ds_read_b128 v[114:117], v0
	ds_read_b128 v[118:121], v0 offset:1024
	ds_read_b128 v[138:141], v0 offset:2048
	ds_read_b128 v[150:153], v0 offset:3072
	v_add_u32_e32 v0, s65, v148
	ds_read_b128 v[154:157], v0
	ds_read_b128 v[158:161], v0 offset:1024
	ds_read_b128 v[170:173], v0 offset:2048
	ds_read_b128 v[174:177], v0 offset:3072
	s_add_u32 s62, s28, 0x80000
	v_mov_b32_e32 v0, v144
	s_mov_b32 m0, s56
	ds_read_b128 v[178:181], v149 offset:32768
	ds_read_b128 v[182:185], v149 offset:33792
	ds_read_b128 v[186:189], v149 offset:34816
	ds_read_b128 v[190:193], v149 offset:35840
	ds_read_b128 v[208:211], v149 offset:36864
	ds_read_b128 v[212:215], v149 offset:37888
	ds_read_b128 v[216:219], v149 offset:38912
	ds_read_b128 v[220:223], v149 offset:39936
	s_addc_u32 s63, s29, 0
	s_nop 0
	global_load_lds_dwordx4 v0, s[62:63]
	v_mov_b32_e32 v0, v146
	s_mov_b32 m0, s57
	s_nop 0
	global_load_lds_dwordx4 v0, s[62:63]
	s_waitcnt vmcnt(8)
	s_waitcnt lgkmcnt(0)
	s_barrier
	s_setprio 1
	s_waitcnt lgkmcnt(0)
	v_mfma_f32_16x16x32_bf16 v[130:133], v[114:117], v[178:181], v[130:133]
	v_mfma_f32_16x16x32_bf16 v[134:137], v[138:141], v[178:181], v[134:137]
	v_mfma_f32_16x16x32_bf16 v[122:125], v[114:117], v[186:189], v[122:125]
	v_mfma_f32_16x16x32_bf16 v[126:129], v[138:141], v[186:189], v[126:129]
	v_mfma_f32_16x16x32_bf16 v[106:109], v[114:117], v[208:211], v[106:109]
	v_mfma_f32_16x16x32_bf16 v[110:113], v[138:141], v[208:211], v[110:113]
	v_mfma_f32_16x16x32_bf16 v[98:101], v[114:117], v[216:219], v[98:101]
	v_mfma_f32_16x16x32_bf16 v[102:105], v[138:141], v[216:219], v[102:105]
	v_mfma_f32_16x16x32_bf16 v[130:133], v[118:121], v[182:185], v[130:133]
	v_mfma_f32_16x16x32_bf16 v[134:137], v[150:153], v[182:185], v[134:137]
	v_mfma_f32_16x16x32_bf16 v[122:125], v[118:121], v[190:193], v[122:125]
	v_mfma_f32_16x16x32_bf16 v[126:129], v[150:153], v[190:193], v[126:129]
	v_mfma_f32_16x16x32_bf16 v[106:109], v[118:121], v[212:215], v[106:109]
	v_mfma_f32_16x16x32_bf16 v[110:113], v[150:153], v[212:215], v[110:113]
	v_mfma_f32_16x16x32_bf16 v[98:101], v[118:121], v[220:223], v[98:101]
	v_mfma_f32_16x16x32_bf16 v[102:105], v[150:153], v[220:223], v[102:105]
	s_setprio 0
	s_setprio 1
	v_mfma_f32_16x16x32_bf16 v[62:65], v[154:157], v[178:181], v[62:65]
	v_mfma_f32_16x16x32_bf16 v[30:33], v[170:173], v[178:181], v[30:33]
	v_mfma_f32_16x16x32_bf16 v[58:61], v[154:157], v[186:189], v[58:61]
	v_mfma_f32_16x16x32_bf16 v[26:29], v[170:173], v[186:189], v[26:29]
	v_mfma_f32_16x16x32_bf16 v[54:57], v[154:157], v[208:211], v[54:57]
	v_mfma_f32_16x16x32_bf16 v[22:25], v[170:173], v[208:211], v[22:25]
	v_mfma_f32_16x16x32_bf16 v[50:53], v[154:157], v[216:219], v[50:53]
	v_mfma_f32_16x16x32_bf16 v[18:21], v[170:173], v[216:219], v[18:21]
	v_mfma_f32_16x16x32_bf16 v[62:65], v[158:161], v[182:185], v[62:65]
	v_mfma_f32_16x16x32_bf16 v[30:33], v[174:177], v[182:185], v[30:33]
	v_mfma_f32_16x16x32_bf16 v[58:61], v[158:161], v[190:193], v[58:61]
	v_mfma_f32_16x16x32_bf16 v[26:29], v[174:177], v[190:193], v[26:29]
	v_mfma_f32_16x16x32_bf16 v[54:57], v[158:161], v[212:215], v[54:57]
	v_mfma_f32_16x16x32_bf16 v[22:25], v[174:177], v[212:215], v[22:25]
	v_mfma_f32_16x16x32_bf16 v[50:53], v[158:161], v[220:223], v[50:53]
	v_mfma_f32_16x16x32_bf16 v[18:21], v[174:177], v[220:223], v[18:21]
	s_setprio 0
	s_barrier
; #define PG8_STAGE(bufoff, gbase, voff) do { _Pragma("unroll") for (int _i = 0; _i < 2; ++_i) { unsigned _vo = (voff)[_i]; asm volatile("" : "+v"(_vo));     \
;         __builtin_amdgcn_global_load_lds((const unsigned*)((const char*)(gbase) + _vo), (PG8_LAS unsigned*)(lds + (bufoff) + ldsw + _i * 8192), 16, 0, 0); } } while (0)
; #define PG8_WAIT_V(n) asm volatile("s_waitcnt vmcnt(" #n ")" ::: "memory")
; #define PG8_WAIT_L(n) asm volatile("s_waitcnt lgkmcnt(" #n ")" ::: "memory")
; #define PG8_BAR __builtin_amdgcn_s_barrier()
; template <class Epi, class Sched, bool ALIGN_EPI = false, bool SP2 = false, bool FP8 = false>
; __device__ __forceinline__ void gemm_phase(PG8_LAS unsigned char* lds, const Gemm g, const Sched& S, const Epi& E, const int wave_) {
;     ...
;             PG8_LDA(At, 1, 1); PG8_STAGE(PG8_SB(1, 0), b3, voffB); PG8_STAGE(PG8_SB(1, 1), b3 + hstep, voffB); PG8_STAGE(PG8_SA(1, 0), a3, voffA);
;             PG8_WAIT_V(8); PG8_WAIT_L(0); PG8_BAR; PG8_MMA(1, 0, At, B0); PG8_MMA(1, 1, At, B1); PG8_BAR; PG8_SCHED;
;             } else {
;             PG8_LDB(B0, 0, 0); PG8_SCHED; PG8_LDA(At, 0, 0); PG8_STAGE(PG8_SA(1, 1), a1 + hstep, voffA);
;             PG8_WAIT_L(8); PG8_BAR; PG8_WAIT_L(0); PG8_MMA(0, 0, At, B0); PG8_BAR; PG8_SCHED;
;             PG8_LDB(B1, 0, 1); PG8_STAGE(PG8_SB(0, 0), b2, voffB);
;             PG8_BAR; PG8_WAIT_L(0); PG8_MMA(0, 1, At, B1); PG8_BAR;
;             PG8_LDA(At, 0, 1); PG8_STAGE(PG8_SA(0, 0), a2, voffA);
;             PG8_BAR; PG8_WAIT_L(0); PG8_MMA(1, 0, At, B0); PG8_BAR; PG8_SCHED;
;             PG8_STAGE(PG8_SB(0, 1), b2 + hstep, voffB);
;             PG8_WAIT_V(6); PG8_BAR; PG8_MMA(1, 1, At, B1); PG8_BAR;
;             PG8_LDB(B0, 1, 0); PG8_SCHED; PG8_LDA(At, 1, 0); PG8_STAGE(PG8_SA(0, 1), a2 + hstep, voffA);
;             PG8_WAIT_L(8); PG8_BAR; PG8_WAIT_L(0); PG8_MMA(0, 0, At, B0); PG8_BAR; PG8_SCHED;
;             PG8_LDB(B1, 1, 1); PG8_STAGE(PG8_SB(1, 0), b3, voffB);
;             PG8_BAR; PG8_WAIT_L(0); PG8_MMA(0, 1, At, B1); PG8_BAR;
;             PG8_LDA(At, 1, 1); PG8_STAGE(PG8_SA(1, 0), a3, voffA);
;             PG8_BAR; PG8_WAIT_L(0); PG8_MMA(1, 0, At, B0); PG8_BAR; PG8_SCHED;
;             PG8_STAGE(PG8_SB(1, 1), b3 + hstep, voffB);
;             PG8_WAIT_V(6); PG8_BAR; PG8_MMA(1, 1, At, B1); PG8_BAR;
;             }
;         }
;         if constexpr (ALIGN_EPI) { if (wr == 0) PG8_BAR; }
	v_mov_b32_e32 v0, v145
	ds_read_b128 v[178:181], v149 offset:49152
	ds_read_b128 v[182:185], v149 offset:50176
	ds_read_b128 v[186:189], v149 offset:51200
	ds_read_b128 v[190:193], v149 offset:52224
	ds_read_b128 v[208:211], v149 offset:53248
	ds_read_b128 v[212:215], v149 offset:54272
	ds_read_b128 v[216:219], v149 offset:55296
	ds_read_b128 v[220:223], v149 offset:56320
	s_add_i32 s62, s64, s33
	s_add_u32 s98, s34, s6
	s_addc_u32 s99, s35, s7
	s_mov_b32 m0, s62
	v_mov_b32_e32 v0, v147
	global_load_lds_dwordx4 v145, s[98:99]
	s_add_i32 m0, s62, 0x2000
	s_nop 0
	s_add_u32 s98, s34, s6
	s_addc_u32 s99, s35, s7
	s_add_u32 s34, s34, 0x80080
	s_addc_u32 s35, s35, 0
	v_mov_b32_e32 v0, v145
	s_add_i32 s62, s65, s33
	global_load_lds_dwordx4 v147, s[98:99]
	s_mov_b32 m0, s62
	s_nop 0
	global_load_lds_dwordx4 v0, s[34:35]
	v_mov_b32_e32 v0, v147
	s_add_i32 m0, s62, 0x2000
	s_nop 0
	global_load_lds_dwordx4 v0, s[34:35]
	v_mov_b32_e32 v0, v144
	s_mov_b32 m0, s58
	s_add_u32 s98, s28, s6
	s_addc_u32 s99, s29, s7
	v_mov_b32_e32 v0, v146
	global_load_lds_dwordx4 v144, s[98:99]
	s_mov_b32 m0, s59
	s_add_u32 s98, s28, s6
	s_addc_u32 s99, s29, s7
	global_load_lds_dwordx4 v146, s[98:99]
	s_waitcnt vmcnt(8)
	s_waitcnt lgkmcnt(0)
	s_barrier
	s_setprio 1
	s_waitcnt lgkmcnt(0)
	v_mfma_f32_16x16x32_bf16 v[90:93], v[114:117], v[178:181], v[90:93]
	v_mfma_f32_16x16x32_bf16 v[94:97], v[138:141], v[178:181], v[94:97]
	v_mfma_f32_16x16x32_bf16 v[82:85], v[114:117], v[186:189], v[82:85]
	v_mfma_f32_16x16x32_bf16 v[86:89], v[138:141], v[186:189], v[86:89]
	v_mfma_f32_16x16x32_bf16 v[74:77], v[114:117], v[208:211], v[74:77]
	v_mfma_f32_16x16x32_bf16 v[78:81], v[138:141], v[208:211], v[78:81]
	v_mfma_f32_16x16x32_bf16 v[66:69], v[114:117], v[216:219], v[66:69]
	v_mfma_f32_16x16x32_bf16 v[70:73], v[138:141], v[216:219], v[70:73]
	v_mfma_f32_16x16x32_bf16 v[90:93], v[118:121], v[182:185], v[90:93]
	v_mfma_f32_16x16x32_bf16 v[94:97], v[150:153], v[182:185], v[94:97]
	v_mfma_f32_16x16x32_bf16 v[82:85], v[118:121], v[190:193], v[82:85]
	v_mfma_f32_16x16x32_bf16 v[86:89], v[150:153], v[190:193], v[86:89]
	v_mfma_f32_16x16x32_bf16 v[74:77], v[118:121], v[212:215], v[74:77]
	v_mfma_f32_16x16x32_bf16 v[78:81], v[150:153], v[212:215], v[78:81]
	v_mfma_f32_16x16x32_bf16 v[66:69], v[118:121], v[220:223], v[66:69]
	v_mfma_f32_16x16x32_bf16 v[70:73], v[150:153], v[220:223], v[70:73]
	s_setprio 0
	s_setprio 1
	v_mfma_f32_16x16x32_bf16 v[46:49], v[154:157], v[178:181], v[46:49]
	v_mfma_f32_16x16x32_bf16 v[14:17], v[170:173], v[178:181], v[14:17]
	v_mfma_f32_16x16x32_bf16 v[42:45], v[154:157], v[186:189], v[42:45]
	v_mfma_f32_16x16x32_bf16 v[10:13], v[170:173], v[186:189], v[10:13]
	v_mfma_f32_16x16x32_bf16 v[38:41], v[154:157], v[208:211], v[38:41]
	v_mfma_f32_16x16x32_bf16 v[6:9], v[170:173], v[208:211], v[6:9]
	v_mfma_f32_16x16x32_bf16 v[34:37], v[154:157], v[216:219], v[34:37]
	v_mfma_f32_16x16x32_bf16 v[2:5], v[170:173], v[216:219], v[2:5]
	v_mfma_f32_16x16x32_bf16 v[46:49], v[158:161], v[182:185], v[46:49]
	v_mfma_f32_16x16x32_bf16 v[14:17], v[174:177], v[182:185], v[14:17]
	v_mfma_f32_16x16x32_bf16 v[42:45], v[158:161], v[190:193], v[42:45]
	v_mfma_f32_16x16x32_bf16 v[10:13], v[174:177], v[190:193], v[10:13]
	v_mfma_f32_16x16x32_bf16 v[38:41], v[158:161], v[212:215], v[38:41]
	v_mfma_f32_16x16x32_bf16 v[6:9], v[174:177], v[212:215], v[6:9]
	v_mfma_f32_16x16x32_bf16 v[34:37], v[158:161], v[220:223], v[34:37]
	v_mfma_f32_16x16x32_bf16 v[2:5], v[174:177], v[220:223], v[2:5]
	s_setprio 0
	s_barrier
	s_add_i32 s47, s47, 2
	s_add_u32 s26, s26, 0x100
	s_addc_u32 s27, s27, 0
	s_add_u32 s45, s45, 0x100
	s_addc_u32 s46, s46, 0
	s_cmp_gt_u32 s47, 29
	s_cbranch_scc0 .LBB0_169
	v_readlane_b32 s18, v252, 10
	v_readlane_b32 s19, v252, 11
	s_and_b64 vcc, exec, s[18:19]
	s_cbranch_vccz .LBB0_172
	s_barrier

; #define PG8_STAGE(bufoff, gbase, voff) do { _Pragma("unroll") for (int _i = 0; _i < 2; ++_i) { unsigned _vo = (voff)[_i]; asm volatile("" : "+v"(_vo));     \
;         __builtin_amdgcn_global_load_lds((const unsigned*)((const char*)(gbase) + _vo), (PG8_LAS unsigned*)(lds + (bufoff) + ldsw + _i * 8192), 16, 0, 0); } } while (0)
; #define PG8_LDA(dst, b, h) do { _Pragma("unroll") for (int m = 0; m < 4; ++m) _Pragma("unroll") for (int k = 0; k < 2; ++k) dst[m][k] = *(const PG8_LAS bf16x8*)(lds + PG8_SA(b, h) + aoff + m * 2048 + k * 1024); } while (0)
; #define PG8_LDB(dst, b, h) do { _Pragma("unroll") for (int n = 0; n < 2; ++n) _Pragma("unroll") for (int k = 0; k < 2; ++k) dst[n][k] = *(const PG8_LAS bf16x8*)(lds + PG8_SB(b, h) + boff + n * 2048 + k * 1024); } while (0)
; #define PG8_WAIT_V(n) asm volatile("s_waitcnt vmcnt(" #n ")" ::: "memory")
; #define PG8_WAIT_L(n) asm volatile("s_waitcnt lgkmcnt(" #n ")" ::: "memory")
; #define PG8_BAR __builtin_amdgcn_s_barrier()
; #define PG8_SCHED __builtin_amdgcn_sched_barrier(0)
; template <class Epi, class Sched, bool ALIGN_EPI = false, bool SP2 = false, bool FP8 = false>
; __device__ __forceinline__ void gemm_phase(PG8_LAS unsigned char* lds, const Gemm g, const Sched& S, const Epi& E, const int wave_) {
;     ...
;         for (int t = 0; t < ntc; t += 2) {
;             const bool last = (t == ntc - 2);
;             const char* a1 = cA + (size_t)(t + 1) * kstep;
;             const char* a2 = last ? nA : cA + (size_t)(t + 2) * kstep; const char* b2 = last ? nB : cB + (size_t)(t + 2) * kstep;
;             const char* a3 = a2 + kstep; const char* b3 = b2 + kstep;
;             if (last && has_next) S.a_ready(nxt);
;             if constexpr (SP2) {
;             PG8_LDB(B0, 0, 0); PG8_LDB(B1, 0, 1); PG8_SCHED; PG8_LDA(At, 0, 0); PG8_STAGE(PG8_SA(1, 1), a1 + hstep, voffA);
;             PG8_WAIT_V(8); PG8_WAIT_L(0); PG8_BAR; PG8_MMA(0, 0, At, B0); PG8_MMA(0, 1, At, B1); PG8_BAR; PG8_SCHED;
;             PG8_LDA(At, 0, 1); PG8_STAGE(PG8_SB(0, 0), b2, voffB); PG8_STAGE(PG8_SB(0, 1), b2 + hstep, voffB); PG8_STAGE(PG8_SA(0, 0), a2, voffA);
;             PG8_WAIT_V(8); PG8_WAIT_L(0); PG8_BAR; PG8_MMA(1, 0, At, B0); PG8_MMA(1, 1, At, B1); PG8_BAR; PG8_SCHED;
.LBB0_274:
	s_add_u32 s34, s28, 0xfffc0080
	s_addc_u32 s35, s29, -1
	s_add_i32 s62, 0, 0x10000
	s_cmp_eq_u32 s61, 12
	s_cselect_b32 s35, s18, s35
	s_cselect_b32 s34, s19, s34
	v_add_u32_e32 v0, s62, v212
	s_cselect_b32 s43, s21, s60
	s_cselect_b32 s42, s23, s45
	s_add_i32 s64, 0, 0x14000
	ds_read_b128 v[130:133], v0
	ds_read_b128 v[134:137], v0 offset:1024
	ds_read_b128 v[138:141], v0 offset:2048
	ds_read_b128 v[142:145], v0 offset:3072
	v_add_u32_e32 v0, s64, v212
	ds_read_b128 v[146:149], v0
	ds_read_b128 v[150:153], v0 offset:1024
	ds_read_b128 v[154:157], v0 offset:2048
	ds_read_b128 v[158:161], v0 offset:3072
	v_mov_b32_e32 v0, v200
	ds_read_b128 v[170:173], v213
	ds_read_b128 v[174:177], v213 offset:1024
	ds_read_b128 v[178:181], v213 offset:2048
	ds_read_b128 v[182:185], v213 offset:3072
	ds_read_b128 v[186:189], v213 offset:4096
	ds_read_b128 v[190:193], v213 offset:5120
	ds_read_b128 v[214:217], v213 offset:6144
	ds_read_b128 v[218:221], v213 offset:7168
	s_add_i32 m0, s52, 0xc000
	s_nop 0
	global_load_lds_dwordx4 v0, s[28:29]
	v_mov_b32_e32 v0, v194
	s_add_i32 m0, s52, 0xe000
	s_nop 0
	global_load_lds_dwordx4 v0, s[28:29]
	s_waitcnt vmcnt(8)
	s_waitcnt lgkmcnt(0)
	s_barrier
	s_setprio 1
	s_waitcnt lgkmcnt(0)
	v_mfma_scale_f32_16x16x128_f8f6f4 v[126:129], v[130:137], v[170:177], v[126:129], v203, v202 op_sel_hi:[0,0,0]
	v_mfma_scale_f32_16x16x128_f8f6f4 v[122:125], v[138:145], v[170:177], v[122:125], v203, v202 op_sel_hi:[0,0,0]
	v_mfma_scale_f32_16x16x128_f8f6f4 v[110:113], v[130:137], v[178:185], v[110:113], v203, v202 op_sel_hi:[0,0,0]
	v_mfma_scale_f32_16x16x128_f8f6f4 v[106:109], v[138:145], v[178:185], v[106:109], v203, v202 op_sel_hi:[0,0,0]
	v_mfma_scale_f32_16x16x128_f8f6f4 v[222:225], v[130:137], v[186:193], v[94:97], v203, v202 op_sel_hi:[0,0,0]
	v_mfma_scale_f32_16x16x128_f8f6f4 v[226:229], v[138:145], v[186:193], v[90:93], v203, v202 op_sel_hi:[0,0,0]
	v_mfma_scale_f32_16x16x128_f8f6f4 v[230:233], v[130:137], v[214:221], v[78:81], v203, v202 op_sel_hi:[0,0,0]
	v_mfma_scale_f32_16x16x128_f8f6f4 v[234:237], v[138:145], v[214:221], v[74:77], v203, v202 op_sel_hi:[0,0,0]
	s_setprio 0
	s_setprio 1
	v_mfma_scale_f32_16x16x128_f8f6f4 v[118:121], v[146:153], v[170:177], v[118:121], v203, v202 op_sel_hi:[0,0,0]
	v_mfma_scale_f32_16x16x128_f8f6f4 v[114:117], v[154:161], v[170:177], v[114:117], v203, v202 op_sel_hi:[0,0,0]
	v_mfma_scale_f32_16x16x128_f8f6f4 v[102:105], v[146:153], v[178:185], v[102:105], v203, v202 op_sel_hi:[0,0,0]
	v_mfma_scale_f32_16x16x128_f8f6f4 v[98:101], v[154:161], v[178:185], v[98:101], v203, v202 op_sel_hi:[0,0,0]
	v_mfma_scale_f32_16x16x128_f8f6f4 v[170:173], v[146:153], v[186:193], v[86:89], v203, v202 op_sel_hi:[0,0,0]
	v_mfma_scale_f32_16x16x128_f8f6f4 v[174:177], v[154:161], v[186:193], v[82:85], v203, v202 op_sel_hi:[0,0,0]
	v_mfma_scale_f32_16x16x128_f8f6f4 v[178:181], v[146:153], v[214:221], v[70:73], v203, v202 op_sel_hi:[0,0,0]
	v_mfma_scale_f32_16x16x128_f8f6f4 v[182:185], v[154:161], v[214:221], v[66:69], v203, v202 op_sel_hi:[0,0,0]
	s_setprio 0
	s_barrier
	v_mov_b32_e32 v0, v250
	s_add_i32 s62, s62, s33
	s_nop 2
	ds_read_b128 v[66:69], v213 offset:16384
	ds_read_b128 v[70:73], v213 offset:17408
	ds_read_b128 v[74:77], v213 offset:18432
	ds_read_b128 v[78:81], v213 offset:19456
	ds_read_b128 v[82:85], v213 offset:20480
	ds_read_b128 v[86:89], v213 offset:21504
	ds_read_b128 v[90:93], v213 offset:22528
	ds_read_b128 v[94:97], v213 offset:23552
	s_mov_b32 m0, s62
	s_nop 0
	global_load_lds_dwordx4 v0, s[42:43]
	v_mov_b32_e32 v0, v195
	s_add_i32 m0, s62, 0x2000
	s_add_u32 s62, s42, 0x40000
	global_load_lds_dwordx4 v0, s[42:43]
	s_addc_u32 s63, s43, 0
	v_mov_b32_e32 v0, v250
	s_add_i32 s64, s64, s33
	s_mov_b32 m0, s64
	s_nop 0
	global_load_lds_dwordx4 v0, s[62:63]
	v_mov_b32_e32 v0, v195
	s_add_i32 m0, s64, 0x2000
	s_nop 0
	global_load_lds_dwordx4 v0, s[62:63]
	v_mov_b32_e32 v0, v200
	s_mov_b32 m0, s52
	s_nop 0
	global_load_lds_dwordx4 v0, s[34:35]
	v_mov_b32_e32 v0, v194
	s_mov_b32 m0, s53
	s_nop 0
	global_load_lds_dwordx4 v0, s[34:35]
	s_waitcnt vmcnt(8)
	s_waitcnt lgkmcnt(0)
	s_barrier
	s_setprio 1
	s_waitcnt lgkmcnt(0)
	v_mfma_scale_f32_16x16x128_f8f6f4 v[62:65], v[130:137], v[66:73], v[62:65], v203, v202 op_sel_hi:[0,0,0]
	v_mfma_scale_f32_16x16x128_f8f6f4 v[58:61], v[138:145], v[66:73], v[58:61], v203, v202 op_sel_hi:[0,0,0]
	v_mfma_scale_f32_16x16x128_f8f6f4 v[186:189], v[130:137], v[74:81], v[46:49], v203, v202 op_sel_hi:[0,0,0]
	v_mfma_scale_f32_16x16x128_f8f6f4 v[190:193], v[138:145], v[74:81], v[42:45], v203, v202 op_sel_hi:[0,0,0]
	v_mfma_scale_f32_16x16x128_f8f6f4 v[214:217], v[130:137], v[82:89], v[30:33], v203, v202 op_sel_hi:[0,0,0]
	v_mfma_scale_f32_16x16x128_f8f6f4 v[218:221], v[138:145], v[82:89], v[26:29], v203, v202 op_sel_hi:[0,0,0]
	v_mfma_scale_f32_16x16x128_f8f6f4 v[238:241], v[130:137], v[90:97], v[14:17], v203, v202 op_sel_hi:[0,0,0]
	v_mfma_scale_f32_16x16x128_f8f6f4 v[242:245], v[138:145], v[90:97], v[10:13], v203, v202 op_sel_hi:[0,0,0]
	s_setprio 0
	s_setprio 1
	v_mfma_scale_f32_16x16x128_f8f6f4 v[54:57], v[146:153], v[66:73], v[54:57], v203, v202 op_sel_hi:[0,0,0]
	v_mfma_scale_f32_16x16x128_f8f6f4 v[50:53], v[154:161], v[66:73], v[50:53], v203, v202 op_sel_hi:[0,0,0]
	v_mfma_scale_f32_16x16x128_f8f6f4 v[246:249], v[146:153], v[74:81], v[38:41], v203, v202 op_sel_hi:[0,0,0]
	v_mfma_scale_f32_16x16x128_f8f6f4 v[196:199], v[154:161], v[74:81], v[34:37], v203, v202 op_sel_hi:[0,0,0]
	v_mfma_scale_f32_16x16x128_f8f6f4 v[162:165], v[146:153], v[82:89], v[22:25], v203, v202 op_sel_hi:[0,0,0]
	v_mfma_scale_f32_16x16x128_f8f6f4 v[166:169], v[154:161], v[82:89], v[18:21], v203, v202 op_sel_hi:[0,0,0]
	v_mfma_scale_f32_16x16x128_f8f6f4 v[204:207], v[146:153], v[90:97], v[6:9], v203, v202 op_sel_hi:[0,0,0]
	v_mfma_scale_f32_16x16x128_f8f6f4 v[208:211], v[154:161], v[90:97], v[2:5], v203, v202 op_sel_hi:[0,0,0]
	s_setprio 0
	s_barrier
; #define PG8_WAIT_V(n) asm volatile("s_waitcnt vmcnt(" #n ")" ::: "memory")
; #define PG8_WAIT_L(n) asm volatile("s_waitcnt lgkmcnt(" #n ")" ::: "memory")
; template <class Epi, class Sched, bool ALIGN_EPI = false, bool SP2 = false, bool FP8 = false>
; __device__ __forceinline__ void gemm_phase(PG8_LAS unsigned char* lds, const Gemm g, const Sched& S, const Epi& E, const int wave_) {
;     ...
;             PG8_WAIT_V(8); PG8_WAIT_L(0); PG8_BAR; PG8_MMA(1, 0, At, B0); PG8_MMA(1, 1, At, B1); PG8_BAR; PG8_SCHED;
;             PG8_LDB(B0, 1, 0); PG8_LDB(B1, 1, 1); PG8_SCHED; PG8_LDA(At, 1, 0); PG8_STAGE(PG8_SA(0, 1), a2 + hstep, voffA);
;             PG8_WAIT_V(8); PG8_WAIT_L(0); PG8_BAR; PG8_MMA(0, 0, At, B0); PG8_MMA(0, 1, At, B1); PG8_BAR; PG8_SCHED;
;             PG8_LDA(At, 1, 1); PG8_STAGE(PG8_SB(1, 0), b3, voffB); PG8_STAGE(PG8_SB(1, 1), b3 + hstep, voffB); PG8_STAGE(PG8_SA(1, 0), a3, voffA);
;             PG8_WAIT_V(8); PG8_WAIT_L(0); PG8_BAR; PG8_MMA(1, 0, At, B0); PG8_MMA(1, 1, At, B1); PG8_BAR; PG8_SCHED;
;             } else {
;             PG8_LDB(B0, 0, 0); PG8_SCHED; PG8_LDA(At, 0, 0); PG8_STAGE(PG8_SA(1, 1), a1 + hstep, voffA);
;             PG8_WAIT_L(8); PG8_BAR; PG8_WAIT_L(0); PG8_MMA(0, 0, At, B0); PG8_BAR; PG8_SCHED;
;             PG8_LDB(B1, 0, 1); PG8_STAGE(PG8_SB(0, 0), b2, voffB);
;             PG8_BAR; PG8_WAIT_L(0); PG8_MMA(0, 1, At, B1); PG8_BAR;
;             PG8_LDA(At, 0, 1); PG8_STAGE(PG8_SA(0, 0), a2, voffA);
;             PG8_BAR; PG8_WAIT_L(0); PG8_MMA(1, 0, At, B0); PG8_BAR; PG8_SCHED;
;             PG8_STAGE(PG8_SB(0, 1), b2 + hstep, voffB);
;             PG8_WAIT_V(6); PG8_BAR; PG8_MMA(1, 1, At, B1); PG8_BAR;
;             PG8_LDB(B0, 1, 0); PG8_SCHED; PG8_LDA(At, 1, 0); PG8_STAGE(PG8_SA(0, 1), a2 + hstep, voffA);
;             PG8_WAIT_L(8); PG8_BAR; PG8_WAIT_L(0); PG8_MMA(0, 0, At, B0); PG8_BAR; PG8_SCHED;
;             PG8_LDB(B1, 1, 1); PG8_STAGE(PG8_SB(1, 0), b3, voffB);
;             PG8_BAR; PG8_WAIT_L(0); PG8_MMA(0, 1, At, B1); PG8_BAR;
;             PG8_LDA(At, 1, 1); PG8_STAGE(PG8_SA(1, 0), a3, voffA);
;             PG8_BAR; PG8_WAIT_L(0); PG8_MMA(1, 0, At, B0); PG8_BAR; PG8_SCHED;
;             PG8_STAGE(PG8_SB(1, 1), b3 + hstep, voffB);
;             PG8_WAIT_V(6); PG8_BAR; PG8_MMA(1, 1, At, B1); PG8_BAR;
;             }
;         }
;         if constexpr (ALIGN_EPI) { if (wr == 0) PG8_BAR; }
	s_add_i32 s64, 0, 0x18000
	v_add_u32_e32 v0, s64, v212
	s_add_i32 s65, 0, 0x1c000
	s_nop 1
	ds_read_b128 v[2:5], v0
	ds_read_b128 v[6:9], v0 offset:1024
	ds_read_b128 v[18:21], v0 offset:2048
	ds_read_b128 v[22:25], v0 offset:3072
	v_add_u32_e32 v0, s65, v212
	ds_read_b128 v[130:133], v0
	ds_read_b128 v[134:137], v0 offset:1024
	ds_read_b128 v[138:141], v0 offset:2048
	ds_read_b128 v[142:145], v0 offset:3072
	s_add_u32 s62, s34, 0x40000
	v_mov_b32_e32 v0, v200
	s_mov_b32 m0, s54
	ds_read_b128 v[10:13], v213 offset:32768
	ds_read_b128 v[14:17], v213 offset:33792
	ds_read_b128 v[26:29], v213 offset:34816
	ds_read_b128 v[30:33], v213 offset:35840
	ds_read_b128 v[34:37], v213 offset:36864
	ds_read_b128 v[38:41], v213 offset:37888
	ds_read_b128 v[42:45], v213 offset:38912
	ds_read_b128 v[46:49], v213 offset:39936
	s_addc_u32 s63, s35, 0
	s_nop 0
	global_load_lds_dwordx4 v0, s[62:63]
	v_mov_b32_e32 v0, v194
	s_mov_b32 m0, s55
	s_nop 0
	global_load_lds_dwordx4 v0, s[62:63]
	s_waitcnt vmcnt(8)
	s_waitcnt lgkmcnt(0)
	s_barrier
	s_setprio 1
	s_waitcnt lgkmcnt(0)
	v_mfma_scale_f32_16x16x128_f8f6f4 v[126:129], v[2:9], v[10:17], v[126:129], v203, v202 op_sel_hi:[0,0,0]
	v_mfma_scale_f32_16x16x128_f8f6f4 v[122:125], v[18:25], v[10:17], v[122:125], v203, v202 op_sel_hi:[0,0,0]
	v_mfma_scale_f32_16x16x128_f8f6f4 v[110:113], v[2:9], v[26:33], v[110:113], v203, v202 op_sel_hi:[0,0,0]
	v_mfma_scale_f32_16x16x128_f8f6f4 v[106:109], v[18:25], v[26:33], v[106:109], v203, v202 op_sel_hi:[0,0,0]
	v_mfma_scale_f32_16x16x128_f8f6f4 v[94:97], v[2:9], v[34:41], v[222:225], v203, v202 op_sel_hi:[0,0,0]
	v_mfma_scale_f32_16x16x128_f8f6f4 v[90:93], v[18:25], v[34:41], v[226:229], v203, v202 op_sel_hi:[0,0,0]
	v_mfma_scale_f32_16x16x128_f8f6f4 v[78:81], v[2:9], v[42:49], v[230:233], v203, v202 op_sel_hi:[0,0,0]
	v_mfma_scale_f32_16x16x128_f8f6f4 v[74:77], v[18:25], v[42:49], v[234:237], v203, v202 op_sel_hi:[0,0,0]
	s_setprio 0
	s_setprio 1
	v_mfma_scale_f32_16x16x128_f8f6f4 v[118:121], v[130:137], v[10:17], v[118:121], v203, v202 op_sel_hi:[0,0,0]
	v_mfma_scale_f32_16x16x128_f8f6f4 v[114:117], v[138:145], v[10:17], v[114:117], v203, v202 op_sel_hi:[0,0,0]
	v_mfma_scale_f32_16x16x128_f8f6f4 v[102:105], v[130:137], v[26:33], v[102:105], v203, v202 op_sel_hi:[0,0,0]
	v_mfma_scale_f32_16x16x128_f8f6f4 v[98:101], v[138:145], v[26:33], v[98:101], v203, v202 op_sel_hi:[0,0,0]
	v_mfma_scale_f32_16x16x128_f8f6f4 v[86:89], v[130:137], v[34:41], v[170:173], v203, v202 op_sel_hi:[0,0,0]
	v_mfma_scale_f32_16x16x128_f8f6f4 v[82:85], v[138:145], v[34:41], v[174:177], v203, v202 op_sel_hi:[0,0,0]
	v_mfma_scale_f32_16x16x128_f8f6f4 v[70:73], v[130:137], v[42:49], v[178:181], v203, v202 op_sel_hi:[0,0,0]
	v_mfma_scale_f32_16x16x128_f8f6f4 v[66:69], v[138:145], v[42:49], v[182:185], v203, v202 op_sel_hi:[0,0,0]
	s_setprio 0
	s_barrier
	v_mov_b32_e32 v0, v250
	ds_read_b128 v[34:37], v213 offset:49152
	ds_read_b128 v[38:41], v213 offset:50176
	ds_read_b128 v[146:149], v213 offset:51200
	ds_read_b128 v[150:153], v213 offset:52224
	ds_read_b128 v[154:157], v213 offset:53248
	ds_read_b128 v[158:161], v213 offset:54272
	ds_read_b128 v[170:173], v213 offset:55296
	ds_read_b128 v[174:177], v213 offset:56320
	s_add_i32 s62, s64, s33
	s_add_u32 s98, s42, s6
	s_addc_u32 s99, s43, s7
	s_mov_b32 m0, s62
	v_mov_b32_e32 v0, v195
	global_load_lds_dwordx4 v250, s[98:99]
	s_add_i32 m0, s62, 0x2000
	s_nop 0
	s_add_u32 s98, s42, s6
	s_addc_u32 s99, s43, s7
	s_add_u32 s42, s42, 0x40080
	s_addc_u32 s43, s43, 0
	v_mov_b32_e32 v0, v250
	s_add_i32 s62, s65, s33
	global_load_lds_dwordx4 v195, s[98:99]
	s_mov_b32 m0, s62
	s_nop 0
	global_load_lds_dwordx4 v0, s[42:43]
	v_mov_b32_e32 v0, v195
	s_add_i32 m0, s62, 0x2000
	s_nop 0
	global_load_lds_dwordx4 v0, s[42:43]
	v_mov_b32_e32 v0, v200
	s_mov_b32 m0, s56
	s_add_u32 s98, s34, s6
	s_addc_u32 s99, s35, s7
	v_mov_b32_e32 v0, v194
	global_load_lds_dwordx4 v200, s[98:99]
	s_mov_b32 m0, s57
	s_add_u32 s98, s34, s6
	s_addc_u32 s99, s35, s7
	global_load_lds_dwordx4 v194, s[98:99]
	s_waitcnt vmcnt(8)
	s_waitcnt lgkmcnt(0)
	s_barrier
	s_setprio 1
	s_waitcnt lgkmcnt(0)
	v_mfma_scale_f32_16x16x128_f8f6f4 v[62:65], v[2:9], v[34:41], v[62:65], v203, v202 op_sel_hi:[0,0,0]
	v_mfma_scale_f32_16x16x128_f8f6f4 v[58:61], v[18:25], v[34:41], v[58:61], v203, v202 op_sel_hi:[0,0,0]
	v_mfma_scale_f32_16x16x128_f8f6f4 v[46:49], v[2:9], v[146:153], v[186:189], v203, v202 op_sel_hi:[0,0,0]
	v_mfma_scale_f32_16x16x128_f8f6f4 v[42:45], v[18:25], v[146:153], v[190:193], v203, v202 op_sel_hi:[0,0,0]
	v_mfma_scale_f32_16x16x128_f8f6f4 v[30:33], v[2:9], v[154:161], v[214:217], v203, v202 op_sel_hi:[0,0,0]
	v_mfma_scale_f32_16x16x128_f8f6f4 v[26:29], v[18:25], v[154:161], v[218:221], v203, v202 op_sel_hi:[0,0,0]
	v_mfma_scale_f32_16x16x128_f8f6f4 v[14:17], v[2:9], v[170:177], v[238:241], v203, v202 op_sel_hi:[0,0,0]
	v_mfma_scale_f32_16x16x128_f8f6f4 v[10:13], v[18:25], v[170:177], v[242:245], v203, v202 op_sel_hi:[0,0,0]
	s_setprio 0
	s_setprio 1
	v_mfma_scale_f32_16x16x128_f8f6f4 v[54:57], v[130:137], v[34:41], v[54:57], v203, v202 op_sel_hi:[0,0,0]
	v_mfma_scale_f32_16x16x128_f8f6f4 v[50:53], v[138:145], v[34:41], v[50:53], v203, v202 op_sel_hi:[0,0,0]
	v_mfma_scale_f32_16x16x128_f8f6f4 v[38:41], v[130:137], v[146:153], v[246:249], v203, v202 op_sel_hi:[0,0,0]
	v_mfma_scale_f32_16x16x128_f8f6f4 v[34:37], v[138:145], v[146:153], v[196:199], v203, v202 op_sel_hi:[0,0,0]
	v_mfma_scale_f32_16x16x128_f8f6f4 v[22:25], v[130:137], v[154:161], v[162:165], v203, v202 op_sel_hi:[0,0,0]
	v_mfma_scale_f32_16x16x128_f8f6f4 v[18:21], v[138:145], v[154:161], v[166:169], v203, v202 op_sel_hi:[0,0,0]
	v_mfma_scale_f32_16x16x128_f8f6f4 v[6:9], v[130:137], v[170:177], v[204:207], v203, v202 op_sel_hi:[0,0,0]
	v_mfma_scale_f32_16x16x128_f8f6f4 v[2:5], v[138:145], v[170:177], v[208:211], v203, v202 op_sel_hi:[0,0,0]
	s_setprio 0
	s_barrier
	s_add_i32 s61, s61, 2
	s_add_u32 s28, s28, 0x100
	s_addc_u32 s29, s29, 0
	s_add_u32 s45, s45, 0x100
	s_addc_u32 s60, s60, 0
	s_cmp_gt_u32 s61, 13
	s_cbranch_scc0 .LBB0_274
	v_readlane_b32 s18, v252, 10
	v_readlane_b32 s19, v252, 11
	s_and_b64 vcc, exec, s[18:19]
	s_cbranch_vccz .LBB0_277
	s_barrier

; #define PG8_STAGE(bufoff, gbase, voff) do { _Pragma("unroll") for (int _i = 0; _i < 2; ++_i) { unsigned _vo = (voff)[_i]; asm volatile("" : "+v"(_vo));     \
;         __builtin_amdgcn_global_load_lds((const unsigned*)((const char*)(gbase) + _vo), (PG8_LAS unsigned*)(lds + (bufoff) + ldsw + _i * 8192), 16, 0, 0); } } while (0)
; #define PG8_LDA(dst, b, h) do { _Pragma("unroll") for (int m = 0; m < 4; ++m) _Pragma("unroll") for (int k = 0; k < 2; ++k) dst[m][k] = *(const PG8_LAS bf16x8*)(lds + PG8_SA(b, h) + aoff + m * 2048 + k * 1024); } while (0)
; #define PG8_LDB(dst, b, h) do { _Pragma("unroll") for (int n = 0; n < 2; ++n) _Pragma("unroll") for (int k = 0; k < 2; ++k) dst[n][k] = *(const PG8_LAS bf16x8*)(lds + PG8_SB(b, h) + boff + n * 2048 + k * 1024); } while (0)
; #define PG8_WAIT_V(n) asm volatile("s_waitcnt vmcnt(" #n ")" ::: "memory")
; #define PG8_WAIT_L(n) asm volatile("s_waitcnt lgkmcnt(" #n ")" ::: "memory")
; #define PG8_BAR __builtin_amdgcn_s_barrier()
; #define PG8_SCHED __builtin_amdgcn_sched_barrier(0)
; template <class Epi, class Sched, bool ALIGN_EPI = false, bool SP2 = false, bool FP8 = false>
; __device__ __forceinline__ void gemm_phase(PG8_LAS unsigned char* lds, const Gemm g, const Sched& S, const Epi& E, const int wave_) {
;     ...
;         for (int t = 0; t < ntc; t += 2) {
;             const bool last = (t == ntc - 2);
;             const char* a1 = cA + (size_t)(t + 1) * kstep;
;             const char* a2 = last ? nA : cA + (size_t)(t + 2) * kstep; const char* b2 = last ? nB : cB + (size_t)(t + 2) * kstep;
;             const char* a3 = a2 + kstep; const char* b3 = b2 + kstep;
;             if (last && has_next) S.a_ready(nxt);
;             if constexpr (SP2) {
;             PG8_LDB(B0, 0, 0); PG8_LDB(B1, 0, 1); PG8_SCHED; PG8_LDA(At, 0, 0); PG8_STAGE(PG8_SA(1, 1), a1 + hstep, voffA);
;             PG8_WAIT_V(8); PG8_WAIT_L(0); PG8_BAR; PG8_MMA(0, 0, At, B0); PG8_MMA(0, 1, At, B1); PG8_BAR; PG8_SCHED;
;             PG8_LDA(At, 0, 1); PG8_STAGE(PG8_SB(0, 0), b2, voffB); PG8_STAGE(PG8_SB(0, 1), b2 + hstep, voffB); PG8_STAGE(PG8_SA(0, 0), a2, voffA);
;             PG8_WAIT_V(8); PG8_WAIT_L(0); PG8_BAR; PG8_MMA(1, 0, At, B0); PG8_MMA(1, 1, At, B1); PG8_BAR; PG8_SCHED;
.LBB0_1306:
	s_add_u32 s34, s28, 0xfff80080
	s_addc_u32 s35, s29, -1
	s_add_i32 s58, 0, 0x10000
	s_cmp_eq_u32 s57, 28
	s_cselect_b32 s35, s18, s35
	s_cselect_b32 s34, s19, s34
	v_add_u32_e32 v0, s58, v150
	s_cselect_b32 s43, s21, s56
	s_cselect_b32 s42, s23, s55
	s_add_i32 s60, 0, 0x14000
	ds_read_b128 v[130:133], v0
	ds_read_b128 v[134:137], v0 offset:1024
	ds_read_b128 v[138:141], v0 offset:2048
	ds_read_b128 v[142:145], v0 offset:3072
	v_add_u32_e32 v0, s60, v150
	ds_read_b128 v[152:155], v0
	ds_read_b128 v[156:159], v0 offset:1024
	ds_read_b128 v[160:163], v0 offset:2048
	ds_read_b128 v[164:167], v0 offset:3072
	v_mov_b32_e32 v0, v146
	ds_read_b128 v[168:171], v151
	ds_read_b128 v[172:175], v151 offset:1024
	ds_read_b128 v[176:179], v151 offset:2048
	ds_read_b128 v[180:183], v151 offset:3072
	ds_read_b128 v[184:187], v151 offset:4096
	ds_read_b128 v[188:191], v151 offset:5120
	ds_read_b128 v[192:195], v151 offset:6144
	ds_read_b128 v[196:199], v151 offset:7168
	s_add_i32 m0, s46, 0xc000
	s_nop 0
	global_load_lds_dwordx4 v0, s[28:29]
	v_mov_b32_e32 v0, v148
	s_add_i32 m0, s46, 0xe000
	s_nop 0
	global_load_lds_dwordx4 v0, s[28:29]
	s_waitcnt vmcnt(8)
	s_waitcnt lgkmcnt(0)
	s_barrier
	s_setprio 1
	s_waitcnt lgkmcnt(0)
	v_mfma_f32_16x16x32_bf16 v[126:129], v[130:133], v[168:171], v[126:129]
	v_mfma_f32_16x16x32_bf16 v[122:125], v[138:141], v[168:171], v[122:125]
	v_mfma_f32_16x16x32_bf16 v[110:113], v[130:133], v[176:179], v[110:113]
	v_mfma_f32_16x16x32_bf16 v[106:109], v[138:141], v[176:179], v[106:109]
	v_mfma_f32_16x16x32_bf16 v[94:97], v[130:133], v[184:187], v[94:97]
	v_mfma_f32_16x16x32_bf16 v[90:93], v[138:141], v[184:187], v[90:93]
	v_mfma_f32_16x16x32_bf16 v[78:81], v[130:133], v[192:195], v[78:81]
	v_mfma_f32_16x16x32_bf16 v[74:77], v[138:141], v[192:195], v[74:77]
	v_mfma_f32_16x16x32_bf16 v[126:129], v[134:137], v[172:175], v[126:129]
	v_mfma_f32_16x16x32_bf16 v[122:125], v[142:145], v[172:175], v[122:125]
	v_mfma_f32_16x16x32_bf16 v[110:113], v[134:137], v[180:183], v[110:113]
	v_mfma_f32_16x16x32_bf16 v[106:109], v[142:145], v[180:183], v[106:109]
	v_mfma_f32_16x16x32_bf16 v[94:97], v[134:137], v[188:191], v[94:97]
	v_mfma_f32_16x16x32_bf16 v[90:93], v[142:145], v[188:191], v[90:93]
	v_mfma_f32_16x16x32_bf16 v[78:81], v[134:137], v[196:199], v[78:81]
	v_mfma_f32_16x16x32_bf16 v[74:77], v[142:145], v[196:199], v[74:77]
	s_setprio 0
	s_setprio 1
	v_mfma_f32_16x16x32_bf16 v[118:121], v[152:155], v[168:171], v[118:121]
	v_mfma_f32_16x16x32_bf16 v[114:117], v[160:163], v[168:171], v[114:117]
	v_mfma_f32_16x16x32_bf16 v[102:105], v[152:155], v[176:179], v[102:105]
	v_mfma_f32_16x16x32_bf16 v[98:101], v[160:163], v[176:179], v[98:101]
	v_mfma_f32_16x16x32_bf16 v[86:89], v[152:155], v[184:187], v[86:89]
	v_mfma_f32_16x16x32_bf16 v[82:85], v[160:163], v[184:187], v[82:85]
	v_mfma_f32_16x16x32_bf16 v[70:73], v[152:155], v[192:195], v[70:73]
	v_mfma_f32_16x16x32_bf16 v[66:69], v[160:163], v[192:195], v[66:69]
	v_mfma_f32_16x16x32_bf16 v[118:121], v[156:159], v[172:175], v[118:121]
	v_mfma_f32_16x16x32_bf16 v[114:117], v[164:167], v[172:175], v[114:117]
	v_mfma_f32_16x16x32_bf16 v[102:105], v[156:159], v[180:183], v[102:105]
	v_mfma_f32_16x16x32_bf16 v[98:101], v[164:167], v[180:183], v[98:101]
	v_mfma_f32_16x16x32_bf16 v[86:89], v[156:159], v[188:191], v[86:89]
	v_mfma_f32_16x16x32_bf16 v[82:85], v[164:167], v[188:191], v[82:85]
	v_mfma_f32_16x16x32_bf16 v[70:73], v[156:159], v[196:199], v[70:73]
	v_mfma_f32_16x16x32_bf16 v[66:69], v[164:167], v[196:199], v[66:69]
	s_setprio 0
	s_barrier
	v_mov_b32_e32 v0, v147
	s_add_i32 s58, s58, s33
	ds_read_b128 v[168:171], v151 offset:16384
	ds_read_b128 v[172:175], v151 offset:17408
	ds_read_b128 v[176:179], v151 offset:18432
	ds_read_b128 v[180:183], v151 offset:19456
	ds_read_b128 v[184:187], v151 offset:20480
	ds_read_b128 v[188:191], v151 offset:21504
	ds_read_b128 v[192:195], v151 offset:22528
	ds_read_b128 v[196:199], v151 offset:23552
	s_mov_b32 m0, s58
	s_nop 0
	global_load_lds_dwordx4 v0, s[42:43]
	v_mov_b32_e32 v0, v149
	s_add_i32 m0, s58, 0x2000
	s_add_u32 s58, s42, 0x80000
	global_load_lds_dwordx4 v0, s[42:43]
	s_addc_u32 s59, s43, 0
	v_mov_b32_e32 v0, v147
	s_add_i32 s60, s60, s33
	s_mov_b32 m0, s60
	s_nop 0
	global_load_lds_dwordx4 v0, s[58:59]
	v_mov_b32_e32 v0, v149
	s_add_i32 m0, s60, 0x2000
	s_nop 0
	global_load_lds_dwordx4 v0, s[58:59]
	v_mov_b32_e32 v0, v146
	s_mov_b32 m0, s46
	s_nop 0
	global_load_lds_dwordx4 v0, s[34:35]
	v_mov_b32_e32 v0, v148
	s_mov_b32 m0, s47
	s_nop 0
	global_load_lds_dwordx4 v0, s[34:35]
	s_waitcnt vmcnt(8)
	s_waitcnt lgkmcnt(0)
	s_barrier
; #define PG8_STAGE(bufoff, gbase, voff) do { _Pragma("unroll") for (int _i = 0; _i < 2; ++_i) { unsigned _vo = (voff)[_i]; asm volatile("" : "+v"(_vo));     \
;         __builtin_amdgcn_global_load_lds((const unsigned*)((const char*)(gbase) + _vo), (PG8_LAS unsigned*)(lds + (bufoff) + ldsw + _i * 8192), 16, 0, 0); } } while (0)
; #define PG8_LDA(dst, b, h) do { _Pragma("unroll") for (int m = 0; m < 4; ++m) _Pragma("unroll") for (int k = 0; k < 2; ++k) dst[m][k] = *(const PG8_LAS bf16x8*)(lds + PG8_SA(b, h) + aoff + m * 2048 + k * 1024); } while (0)
; #define PG8_LDB(dst, b, h) do { _Pragma("unroll") for (int n = 0; n < 2; ++n) _Pragma("unroll") for (int k = 0; k < 2; ++k) dst[n][k] = *(const PG8_LAS bf16x8*)(lds + PG8_SB(b, h) + boff + n * 2048 + k * 1024); } while (0)
; #define PG8_WAIT_V(n) asm volatile("s_waitcnt vmcnt(" #n ")" ::: "memory")
; #define PG8_WAIT_L(n) asm volatile("s_waitcnt lgkmcnt(" #n ")" ::: "memory")
; #define PG8_BAR __builtin_amdgcn_s_barrier()
; #define PG8_SCHED __builtin_amdgcn_sched_barrier(0)
; template <class Epi, class Sched, bool ALIGN_EPI = false, bool SP2 = false, bool FP8 = false>
; __device__ __forceinline__ void gemm_phase(PG8_LAS unsigned char* lds, const Gemm g, const Sched& S, const Epi& E, const int wave_) {
;     ...
;             PG8_WAIT_V(8); PG8_WAIT_L(0); PG8_BAR; PG8_MMA(1, 0, At, B0); PG8_MMA(1, 1, At, B1); PG8_BAR; PG8_SCHED;
;             PG8_LDB(B0, 1, 0); PG8_LDB(B1, 1, 1); PG8_SCHED; PG8_LDA(At, 1, 0); PG8_STAGE(PG8_SA(0, 1), a2 + hstep, voffA);
;             PG8_WAIT_V(8); PG8_WAIT_L(0); PG8_BAR; PG8_MMA(0, 0, At, B0); PG8_MMA(0, 1, At, B1); PG8_BAR; PG8_SCHED;
	s_setprio 1
	s_waitcnt lgkmcnt(0)
	v_mfma_f32_16x16x32_bf16 v[62:65], v[130:133], v[168:171], v[62:65]
	v_mfma_f32_16x16x32_bf16 v[58:61], v[138:141], v[168:171], v[58:61]
	v_mfma_f32_16x16x32_bf16 v[46:49], v[130:133], v[176:179], v[46:49]
	v_mfma_f32_16x16x32_bf16 v[42:45], v[138:141], v[176:179], v[42:45]
	v_mfma_f32_16x16x32_bf16 v[30:33], v[130:133], v[184:187], v[30:33]
	v_mfma_f32_16x16x32_bf16 v[26:29], v[138:141], v[184:187], v[26:29]
	v_mfma_f32_16x16x32_bf16 v[14:17], v[130:133], v[192:195], v[14:17]
	v_mfma_f32_16x16x32_bf16 v[10:13], v[138:141], v[192:195], v[10:13]
	v_mfma_f32_16x16x32_bf16 v[62:65], v[134:137], v[172:175], v[62:65]
	v_mfma_f32_16x16x32_bf16 v[58:61], v[142:145], v[172:175], v[58:61]
	v_mfma_f32_16x16x32_bf16 v[46:49], v[134:137], v[180:183], v[46:49]
	v_mfma_f32_16x16x32_bf16 v[42:45], v[142:145], v[180:183], v[42:45]
	v_mfma_f32_16x16x32_bf16 v[30:33], v[134:137], v[188:191], v[30:33]
	v_mfma_f32_16x16x32_bf16 v[26:29], v[142:145], v[188:191], v[26:29]
	v_mfma_f32_16x16x32_bf16 v[14:17], v[134:137], v[196:199], v[14:17]
	v_mfma_f32_16x16x32_bf16 v[10:13], v[142:145], v[196:199], v[10:13]
	s_setprio 0
	s_setprio 1
	v_mfma_f32_16x16x32_bf16 v[54:57], v[152:155], v[168:171], v[54:57]
	v_mfma_f32_16x16x32_bf16 v[50:53], v[160:163], v[168:171], v[50:53]
	v_mfma_f32_16x16x32_bf16 v[38:41], v[152:155], v[176:179], v[38:41]
	v_mfma_f32_16x16x32_bf16 v[34:37], v[160:163], v[176:179], v[34:37]
	v_mfma_f32_16x16x32_bf16 v[22:25], v[152:155], v[184:187], v[22:25]
	v_mfma_f32_16x16x32_bf16 v[18:21], v[160:163], v[184:187], v[18:21]
	v_mfma_f32_16x16x32_bf16 v[6:9], v[152:155], v[192:195], v[6:9]
	v_mfma_f32_16x16x32_bf16 v[2:5], v[160:163], v[192:195], v[2:5]
	v_mfma_f32_16x16x32_bf16 v[54:57], v[156:159], v[172:175], v[54:57]
	v_mfma_f32_16x16x32_bf16 v[50:53], v[164:167], v[172:175], v[50:53]
	v_mfma_f32_16x16x32_bf16 v[38:41], v[156:159], v[180:183], v[38:41]
	v_mfma_f32_16x16x32_bf16 v[34:37], v[164:167], v[180:183], v[34:37]
	v_mfma_f32_16x16x32_bf16 v[22:25], v[156:159], v[188:191], v[22:25]
	v_mfma_f32_16x16x32_bf16 v[18:21], v[164:167], v[188:191], v[18:21]
	v_mfma_f32_16x16x32_bf16 v[6:9], v[156:159], v[196:199], v[6:9]
	v_mfma_f32_16x16x32_bf16 v[2:5], v[164:167], v[196:199], v[2:5]
	s_setprio 0
	s_barrier
	s_add_i32 s60, 0, 0x18000
	v_add_u32_e32 v0, s60, v150
	s_add_i32 s61, 0, 0x1c000
	ds_read_b128 v[130:133], v0
	ds_read_b128 v[134:137], v0 offset:1024
	ds_read_b128 v[138:141], v0 offset:2048
	ds_read_b128 v[142:145], v0 offset:3072
	v_add_u32_e32 v0, s61, v150
	ds_read_b128 v[152:155], v0
	ds_read_b128 v[156:159], v0 offset:1024
	ds_read_b128 v[160:163], v0 offset:2048
	ds_read_b128 v[164:167], v0 offset:3072
	s_add_u32 s58, s34, 0x80000
	v_mov_b32_e32 v0, v146
	s_mov_b32 m0, s48
	ds_read_b128 v[168:171], v151 offset:32768
	ds_read_b128 v[172:175], v151 offset:33792
	ds_read_b128 v[176:179], v151 offset:34816
	ds_read_b128 v[180:183], v151 offset:35840
	ds_read_b128 v[184:187], v151 offset:36864
	ds_read_b128 v[188:191], v151 offset:37888
	ds_read_b128 v[192:195], v151 offset:38912
	ds_read_b128 v[196:199], v151 offset:39936
	s_addc_u32 s59, s35, 0
	s_nop 0
	global_load_lds_dwordx4 v0, s[58:59]
	v_mov_b32_e32 v0, v148
	s_mov_b32 m0, s49
	s_nop 0
	global_load_lds_dwordx4 v0, s[58:59]
	s_waitcnt vmcnt(8)
	s_waitcnt lgkmcnt(0)
	s_barrier
	s_setprio 1
	s_waitcnt lgkmcnt(0)
	v_mfma_f32_16x16x32_bf16 v[126:129], v[130:133], v[168:171], v[126:129]
	v_mfma_f32_16x16x32_bf16 v[122:125], v[138:141], v[168:171], v[122:125]
	v_mfma_f32_16x16x32_bf16 v[110:113], v[130:133], v[176:179], v[110:113]
	v_mfma_f32_16x16x32_bf16 v[106:109], v[138:141], v[176:179], v[106:109]
	v_mfma_f32_16x16x32_bf16 v[94:97], v[130:133], v[184:187], v[94:97]
	v_mfma_f32_16x16x32_bf16 v[90:93], v[138:141], v[184:187], v[90:93]
	v_mfma_f32_16x16x32_bf16 v[78:81], v[130:133], v[192:195], v[78:81]
	v_mfma_f32_16x16x32_bf16 v[74:77], v[138:141], v[192:195], v[74:77]
	v_mfma_f32_16x16x32_bf16 v[126:129], v[134:137], v[172:175], v[126:129]
	v_mfma_f32_16x16x32_bf16 v[122:125], v[142:145], v[172:175], v[122:125]
	v_mfma_f32_16x16x32_bf16 v[110:113], v[134:137], v[180:183], v[110:113]
	v_mfma_f32_16x16x32_bf16 v[106:109], v[142:145], v[180:183], v[106:109]
	v_mfma_f32_16x16x32_bf16 v[94:97], v[134:137], v[188:191], v[94:97]
	v_mfma_f32_16x16x32_bf16 v[90:93], v[142:145], v[188:191], v[90:93]
	v_mfma_f32_16x16x32_bf16 v[78:81], v[134:137], v[196:199], v[78:81]
	v_mfma_f32_16x16x32_bf16 v[74:77], v[142:145], v[196:199], v[74:77]
	s_setprio 0
	s_setprio 1
	v_mfma_f32_16x16x32_bf16 v[118:121], v[152:155], v[168:171], v[118:121]
	v_mfma_f32_16x16x32_bf16 v[114:117], v[160:163], v[168:171], v[114:117]
	v_mfma_f32_16x16x32_bf16 v[102:105], v[152:155], v[176:179], v[102:105]
	v_mfma_f32_16x16x32_bf16 v[98:101], v[160:163], v[176:179], v[98:101]
	v_mfma_f32_16x16x32_bf16 v[86:89], v[152:155], v[184:187], v[86:89]
	v_mfma_f32_16x16x32_bf16 v[82:85], v[160:163], v[184:187], v[82:85]
	v_mfma_f32_16x16x32_bf16 v[70:73], v[152:155], v[192:195], v[70:73]
	v_mfma_f32_16x16x32_bf16 v[66:69], v[160:163], v[192:195], v[66:69]
	v_mfma_f32_16x16x32_bf16 v[118:121], v[156:159], v[172:175], v[118:121]
	v_mfma_f32_16x16x32_bf16 v[114:117], v[164:167], v[172:175], v[114:117]
	v_mfma_f32_16x16x32_bf16 v[102:105], v[156:159], v[180:183], v[102:105]
	v_mfma_f32_16x16x32_bf16 v[98:101], v[164:167], v[180:183], v[98:101]
	v_mfma_f32_16x16x32_bf16 v[86:89], v[156:159], v[188:191], v[86:89]
	v_mfma_f32_16x16x32_bf16 v[82:85], v[164:167], v[188:191], v[82:85]
	v_mfma_f32_16x16x32_bf16 v[70:73], v[156:159], v[196:199], v[70:73]
	v_mfma_f32_16x16x32_bf16 v[66:69], v[164:167], v[196:199], v[66:69]
	s_setprio 0
	s_barrier
; #define PG8_STAGE(bufoff, gbase, voff) do { _Pragma("unroll") for (int _i = 0; _i < 2; ++_i) { unsigned _vo = (voff)[_i]; asm volatile("" : "+v"(_vo));     \
;         __builtin_amdgcn_global_load_lds((const unsigned*)((const char*)(gbase) + _vo), (PG8_LAS unsigned*)(lds + (bufoff) + ldsw + _i * 8192), 16, 0, 0); } } while (0)
; #define PG8_WAIT_V(n) asm volatile("s_waitcnt vmcnt(" #n ")" ::: "memory")
; #define PG8_WAIT_L(n) asm volatile("s_waitcnt lgkmcnt(" #n ")" ::: "memory")
; #define PG8_BAR __builtin_amdgcn_s_barrier()
; template <class Epi, class Sched, bool ALIGN_EPI = false, bool SP2 = false, bool FP8 = false>
; __device__ __forceinline__ void gemm_phase(PG8_LAS unsigned char* lds, const Gemm g, const Sched& S, const Epi& E, const int wave_) {
;     ...
;             PG8_LDA(At, 1, 1); PG8_STAGE(PG8_SB(1, 0), b3, voffB); PG8_STAGE(PG8_SB(1, 1), b3 + hstep, voffB); PG8_STAGE(PG8_SA(1, 0), a3, voffA);
;             PG8_WAIT_V(8); PG8_WAIT_L(0); PG8_BAR; PG8_MMA(1, 0, At, B0); PG8_MMA(1, 1, At, B1); PG8_BAR; PG8_SCHED;
;             } else {
;             PG8_LDB(B0, 0, 0); PG8_SCHED; PG8_LDA(At, 0, 0); PG8_STAGE(PG8_SA(1, 1), a1 + hstep, voffA);
;             PG8_WAIT_L(8); PG8_BAR; PG8_WAIT_L(0); PG8_MMA(0, 0, At, B0); PG8_BAR; PG8_SCHED;
;             PG8_LDB(B1, 0, 1); PG8_STAGE(PG8_SB(0, 0), b2, voffB);
;             PG8_BAR; PG8_WAIT_L(0); PG8_MMA(0, 1, At, B1); PG8_BAR;
;             PG8_LDA(At, 0, 1); PG8_STAGE(PG8_SA(0, 0), a2, voffA);
;             PG8_BAR; PG8_WAIT_L(0); PG8_MMA(1, 0, At, B0); PG8_BAR; PG8_SCHED;
;             PG8_STAGE(PG8_SB(0, 1), b2 + hstep, voffB);
;             PG8_WAIT_V(6); PG8_BAR; PG8_MMA(1, 1, At, B1); PG8_BAR;
;             PG8_LDB(B0, 1, 0); PG8_SCHED; PG8_LDA(At, 1, 0); PG8_STAGE(PG8_SA(0, 1), a2 + hstep, voffA);
;             PG8_WAIT_L(8); PG8_BAR; PG8_WAIT_L(0); PG8_MMA(0, 0, At, B0); PG8_BAR; PG8_SCHED;
;             PG8_LDB(B1, 1, 1); PG8_STAGE(PG8_SB(1, 0), b3, voffB);
;             PG8_BAR; PG8_WAIT_L(0); PG8_MMA(0, 1, At, B1); PG8_BAR;
;             PG8_LDA(At, 1, 1); PG8_STAGE(PG8_SA(1, 0), a3, voffA);
;             PG8_BAR; PG8_WAIT_L(0); PG8_MMA(1, 0, At, B0); PG8_BAR; PG8_SCHED;
;             PG8_STAGE(PG8_SB(1, 1), b3 + hstep, voffB);
;             PG8_WAIT_V(6); PG8_BAR; PG8_MMA(1, 1, At, B1); PG8_BAR;
;             }
;         }
;         if constexpr (ALIGN_EPI) { if (wr == 0) PG8_BAR; }
	v_mov_b32_e32 v0, v147
	ds_read_b128 v[168:171], v151 offset:49152
	ds_read_b128 v[172:175], v151 offset:50176
	ds_read_b128 v[176:179], v151 offset:51200
	ds_read_b128 v[180:183], v151 offset:52224
	ds_read_b128 v[184:187], v151 offset:53248
	ds_read_b128 v[188:191], v151 offset:54272
	ds_read_b128 v[192:195], v151 offset:55296
	ds_read_b128 v[196:199], v151 offset:56320
	s_add_i32 s58, s60, s33
	s_add_u32 s98, s42, s6
	s_addc_u32 s99, s43, s7
	s_mov_b32 m0, s58
	v_mov_b32_e32 v0, v149
	global_load_lds_dwordx4 v147, s[98:99]
	s_add_i32 m0, s58, 0x2000
	s_nop 0
	s_add_u32 s98, s42, s6
	s_addc_u32 s99, s43, s7
	s_add_u32 s42, s42, 0x80080
	s_addc_u32 s43, s43, 0
	v_mov_b32_e32 v0, v147
	s_add_i32 s58, s61, s33
	global_load_lds_dwordx4 v149, s[98:99]
	s_mov_b32 m0, s58
	s_nop 0
	global_load_lds_dwordx4 v0, s[42:43]
	v_mov_b32_e32 v0, v149
	s_add_i32 m0, s58, 0x2000
	s_nop 0
	global_load_lds_dwordx4 v0, s[42:43]
	v_mov_b32_e32 v0, v146
	s_mov_b32 m0, s50
	s_add_u32 s98, s34, s6
	s_addc_u32 s99, s35, s7
	v_mov_b32_e32 v0, v148
	global_load_lds_dwordx4 v146, s[98:99]
	s_mov_b32 m0, s51
	s_add_u32 s98, s34, s6
	s_addc_u32 s99, s35, s7
	global_load_lds_dwordx4 v148, s[98:99]
	s_waitcnt vmcnt(8)
	s_waitcnt lgkmcnt(0)
	s_barrier
	s_setprio 1
	s_waitcnt lgkmcnt(0)
	v_mfma_f32_16x16x32_bf16 v[62:65], v[130:133], v[168:171], v[62:65]
	v_mfma_f32_16x16x32_bf16 v[58:61], v[138:141], v[168:171], v[58:61]
	v_mfma_f32_16x16x32_bf16 v[46:49], v[130:133], v[176:179], v[46:49]
	v_mfma_f32_16x16x32_bf16 v[42:45], v[138:141], v[176:179], v[42:45]
	v_mfma_f32_16x16x32_bf16 v[30:33], v[130:133], v[184:187], v[30:33]
	v_mfma_f32_16x16x32_bf16 v[26:29], v[138:141], v[184:187], v[26:29]
	v_mfma_f32_16x16x32_bf16 v[14:17], v[130:133], v[192:195], v[14:17]
	v_mfma_f32_16x16x32_bf16 v[10:13], v[138:141], v[192:195], v[10:13]
	v_mfma_f32_16x16x32_bf16 v[62:65], v[134:137], v[172:175], v[62:65]
	v_mfma_f32_16x16x32_bf16 v[58:61], v[142:145], v[172:175], v[58:61]
	v_mfma_f32_16x16x32_bf16 v[46:49], v[134:137], v[180:183], v[46:49]
	v_mfma_f32_16x16x32_bf16 v[42:45], v[142:145], v[180:183], v[42:45]
	v_mfma_f32_16x16x32_bf16 v[30:33], v[134:137], v[188:191], v[30:33]
	v_mfma_f32_16x16x32_bf16 v[26:29], v[142:145], v[188:191], v[26:29]
	v_mfma_f32_16x16x32_bf16 v[14:17], v[134:137], v[196:199], v[14:17]
	v_mfma_f32_16x16x32_bf16 v[10:13], v[142:145], v[196:199], v[10:13]
	s_setprio 0
	s_setprio 1
	v_mfma_f32_16x16x32_bf16 v[54:57], v[152:155], v[168:171], v[54:57]
	v_mfma_f32_16x16x32_bf16 v[50:53], v[160:163], v[168:171], v[50:53]
	v_mfma_f32_16x16x32_bf16 v[38:41], v[152:155], v[176:179], v[38:41]
	v_mfma_f32_16x16x32_bf16 v[34:37], v[160:163], v[176:179], v[34:37]
	v_mfma_f32_16x16x32_bf16 v[22:25], v[152:155], v[184:187], v[22:25]
	v_mfma_f32_16x16x32_bf16 v[18:21], v[160:163], v[184:187], v[18:21]
	v_mfma_f32_16x16x32_bf16 v[6:9], v[152:155], v[192:195], v[6:9]
	v_mfma_f32_16x16x32_bf16 v[2:5], v[160:163], v[192:195], v[2:5]
	v_mfma_f32_16x16x32_bf16 v[54:57], v[156:159], v[172:175], v[54:57]
	v_mfma_f32_16x16x32_bf16 v[50:53], v[164:167], v[172:175], v[50:53]
	v_mfma_f32_16x16x32_bf16 v[38:41], v[156:159], v[180:183], v[38:41]
	v_mfma_f32_16x16x32_bf16 v[34:37], v[164:167], v[180:183], v[34:37]
	v_mfma_f32_16x16x32_bf16 v[22:25], v[156:159], v[188:191], v[22:25]
	v_mfma_f32_16x16x32_bf16 v[18:21], v[164:167], v[188:191], v[18:21]
	v_mfma_f32_16x16x32_bf16 v[6:9], v[156:159], v[196:199], v[6:9]
	v_mfma_f32_16x16x32_bf16 v[2:5], v[164:167], v[196:199], v[2:5]
	s_setprio 0
	s_barrier
	s_add_i32 s57, s57, 2
	s_add_u32 s28, s28, 0x100
	s_addc_u32 s29, s29, 0
	s_add_u32 s55, s55, 0x100
	s_addc_u32 s56, s56, 0
	s_cmp_gt_u32 s57, 29
	s_cbranch_scc0 .LBB0_1306
	v_readlane_b32 s18, v252, 10
	v_readlane_b32 s19, v252, 11
	s_and_b64 vcc, exec, s[18:19]
	s_cbranch_vccz .LBB0_1309
	s_barrier

; #define PG8_STAGE(bufoff, gbase, voff) do { _Pragma("unroll") for (int _i = 0; _i < 2; ++_i) { unsigned _vo = (voff)[_i]; asm volatile("" : "+v"(_vo));     \
;         __builtin_amdgcn_global_load_lds((const unsigned*)((const char*)(gbase) + _vo), (PG8_LAS unsigned*)(lds + (bufoff) + ldsw + _i * 8192), 16, 0, 0); } } while (0)
; #define PG8_LDA(dst, b, h) do { _Pragma("unroll") for (int m = 0; m < 4; ++m) _Pragma("unroll") for (int k = 0; k < 2; ++k) dst[m][k] = *(const PG8_LAS bf16x8*)(lds + PG8_SA(b, h) + aoff + m * 2048 + k * 1024); } while (0)
; #define PG8_LDB(dst, b, h) do { _Pragma("unroll") for (int n = 0; n < 2; ++n) _Pragma("unroll") for (int k = 0; k < 2; ++k) dst[n][k] = *(const PG8_LAS bf16x8*)(lds + PG8_SB(b, h) + boff + n * 2048 + k * 1024); } while (0)
; #define PG8_WAIT_V(n) asm volatile("s_waitcnt vmcnt(" #n ")" ::: "memory")
; #define PG8_WAIT_L(n) asm volatile("s_waitcnt lgkmcnt(" #n ")" ::: "memory")
; #define PG8_BAR __builtin_amdgcn_s_barrier()
; #define PG8_SCHED __builtin_amdgcn_sched_barrier(0)
; template <class Epi, class Sched, bool ALIGN_EPI = false, bool SP2 = false, bool FP8 = false>
; __device__ __forceinline__ void gemm_phase(PG8_LAS unsigned char* lds, const Gemm g, const Sched& S, const Epi& E, const int wave_) {
;     ...
;         for (int t = 0; t < ntc; t += 2) {
;             const bool last = (t == ntc - 2);
;             const char* a1 = cA + (size_t)(t + 1) * kstep;
;             const char* a2 = last ? nA : cA + (size_t)(t + 2) * kstep; const char* b2 = last ? nB : cB + (size_t)(t + 2) * kstep;
;             const char* a3 = a2 + kstep; const char* b3 = b2 + kstep;
;             if (last && has_next) S.a_ready(nxt);
;             if constexpr (SP2) {
;             PG8_LDB(B0, 0, 0); PG8_LDB(B1, 0, 1); PG8_SCHED; PG8_LDA(At, 0, 0); PG8_STAGE(PG8_SA(1, 1), a1 + hstep, voffA);
;             PG8_WAIT_V(8); PG8_WAIT_L(0); PG8_BAR; PG8_MMA(0, 0, At, B0); PG8_MMA(0, 1, At, B1); PG8_BAR; PG8_SCHED;
;             PG8_LDA(At, 0, 1); PG8_STAGE(PG8_SB(0, 0), b2, voffB); PG8_STAGE(PG8_SB(0, 1), b2 + hstep, voffB); PG8_STAGE(PG8_SA(0, 0), a2, voffA);
;             PG8_WAIT_V(8); PG8_WAIT_L(0); PG8_BAR; PG8_MMA(1, 0, At, B0); PG8_MMA(1, 1, At, B1); PG8_BAR; PG8_SCHED;
.LBB0_1849:
	s_add_u32 s46, s44, 0xfffc0080
	s_addc_u32 s47, s45, -1
	s_add_i32 s73, 0, 0x10000
	s_cmp_eq_u32 s72, 12
	s_cselect_b32 s47, s18, s47
	s_cselect_b32 s46, s19, s46
	v_add_u32_e32 v0, s73, v138
	s_cselect_b32 s49, s15, s71
	s_cselect_b32 s48, s23, s70
	s_add_i32 s76, 0, 0x14000
	ds_read_b128 v[140:143], v0
	ds_read_b128 v[144:147], v0 offset:1024
	ds_read_b128 v[148:151], v0 offset:2048
	ds_read_b128 v[152:155], v0 offset:3072
	v_add_u32_e32 v0, s76, v138
	ds_read_b128 v[170:173], v0
	ds_read_b128 v[174:177], v0 offset:1024
	ds_read_b128 v[178:181], v0 offset:2048
	ds_read_b128 v[182:185], v0 offset:3072
	v_mov_b32_e32 v0, v168
	ds_read_b128 v[186:189], v139
	ds_read_b128 v[190:193], v139 offset:1024
	ds_read_b128 v[208:211], v139 offset:2048
	ds_read_b128 v[212:215], v139 offset:3072
	ds_read_b128 v[216:219], v139 offset:4096
	ds_read_b128 v[220:223], v139 offset:5120
	ds_read_b128 v[224:227], v139 offset:6144
	ds_read_b128 v[228:231], v139 offset:7168
	s_add_i32 m0, s35, 0xc000
	s_nop 0
	global_load_lds_dwordx4 v0, s[44:45]
	v_mov_b32_e32 v0, v248
	s_add_i32 m0, s35, 0xe000
	s_nop 0
	global_load_lds_dwordx4 v0, s[44:45]
	s_waitcnt vmcnt(8)
	s_waitcnt lgkmcnt(0)
	s_barrier
	s_setprio 1
	s_waitcnt lgkmcnt(0)
	v_mfma_scale_f32_16x16x128_f8f6f4 v[126:129], v[140:147], v[186:193], v[126:129], v203, v202 op_sel_hi:[0,0,0]
	v_mfma_scale_f32_16x16x128_f8f6f4 v[118:121], v[148:155], v[186:193], v[118:121], v203, v202 op_sel_hi:[0,0,0]
	v_mfma_scale_f32_16x16x128_f8f6f4 v[110:113], v[140:147], v[208:215], v[110:113], v203, v202 op_sel_hi:[0,0,0]
	v_mfma_scale_f32_16x16x128_f8f6f4 v[102:105], v[148:155], v[208:215], v[102:105], v203, v202 op_sel_hi:[0,0,0]
	v_mfma_scale_f32_16x16x128_f8f6f4 v[130:133], v[140:147], v[216:223], v[94:97], v203, v202 op_sel_hi:[0,0,0]
	v_mfma_scale_f32_16x16x128_f8f6f4 v[156:159], v[148:155], v[216:223], v[86:89], v203, v202 op_sel_hi:[0,0,0]
	v_mfma_scale_f32_16x16x128_f8f6f4 v[160:163], v[140:147], v[224:231], v[78:81], v203, v202 op_sel_hi:[0,0,0]
	v_mfma_scale_f32_16x16x128_f8f6f4 v[164:167], v[148:155], v[224:231], v[70:73], v203, v202 op_sel_hi:[0,0,0]
	s_setprio 0
	s_setprio 1
	v_mfma_scale_f32_16x16x128_f8f6f4 v[122:125], v[170:177], v[186:193], v[122:125], v203, v202 op_sel_hi:[0,0,0]
	v_mfma_scale_f32_16x16x128_f8f6f4 v[114:117], v[178:185], v[186:193], v[114:117], v203, v202 op_sel_hi:[0,0,0]
	v_mfma_scale_f32_16x16x128_f8f6f4 v[106:109], v[170:177], v[208:215], v[106:109], v203, v202 op_sel_hi:[0,0,0]
	v_mfma_scale_f32_16x16x128_f8f6f4 v[98:101], v[178:185], v[208:215], v[98:101], v203, v202 op_sel_hi:[0,0,0]
	v_mfma_scale_f32_16x16x128_f8f6f4 v[194:197], v[170:177], v[224:231], v[194:197], v203, v202 op_sel_hi:[0,0,0]
	v_mfma_scale_f32_16x16x128_f8f6f4 v[204:207], v[178:185], v[224:231], v[204:207], v203, v202 op_sel_hi:[0,0,0]
	v_mfma_scale_f32_16x16x128_f8f6f4 v[186:189], v[170:177], v[216:223], v[90:93], v203, v202 op_sel_hi:[0,0,0]
	v_mfma_scale_f32_16x16x128_f8f6f4 v[190:193], v[178:185], v[216:223], v[82:85], v203, v202 op_sel_hi:[0,0,0]
	s_setprio 0
	s_barrier
	v_mov_b32_e32 v0, v169
	s_add_i32 s73, s73, s33
	ds_read_b128 v[66:69], v139 offset:16384
	ds_read_b128 v[70:73], v139 offset:17408
	ds_read_b128 v[74:77], v139 offset:18432
	ds_read_b128 v[78:81], v139 offset:19456
	ds_read_b128 v[82:85], v139 offset:20480
	ds_read_b128 v[86:89], v139 offset:21504
	ds_read_b128 v[90:93], v139 offset:22528
	ds_read_b128 v[94:97], v139 offset:23552
	s_mov_b32 m0, s73
	s_nop 0
	global_load_lds_dwordx4 v0, s[48:49]
	v_mov_b32_e32 v0, v249
	s_add_i32 m0, s73, 0x2000
	s_add_u32 s74, s48, 0x40000
	global_load_lds_dwordx4 v0, s[48:49]
	s_addc_u32 s75, s49, 0
	v_mov_b32_e32 v0, v169
	s_add_i32 s73, s76, s33
	s_mov_b32 m0, s73
	s_nop 0
	global_load_lds_dwordx4 v0, s[74:75]
	v_mov_b32_e32 v0, v249
	s_add_i32 m0, s73, 0x2000
	s_nop 0
	global_load_lds_dwordx4 v0, s[74:75]
	v_mov_b32_e32 v0, v168
	s_mov_b32 m0, s35
	s_nop 0
	global_load_lds_dwordx4 v0, s[46:47]
	v_mov_b32_e32 v0, v248
	s_mov_b32 m0, s43
	s_nop 0
	global_load_lds_dwordx4 v0, s[46:47]
	s_waitcnt vmcnt(8)
	s_waitcnt lgkmcnt(0)
	s_barrier
	s_setprio 1
	s_waitcnt lgkmcnt(0)
	v_mfma_scale_f32_16x16x128_f8f6f4 v[62:65], v[140:147], v[66:73], v[62:65], v203, v202 op_sel_hi:[0,0,0]
	v_mfma_scale_f32_16x16x128_f8f6f4 v[54:57], v[148:155], v[66:73], v[54:57], v203, v202 op_sel_hi:[0,0,0]
	v_mfma_scale_f32_16x16x128_f8f6f4 v[46:49], v[140:147], v[74:81], v[46:49], v203, v202 op_sel_hi:[0,0,0]
	v_mfma_scale_f32_16x16x128_f8f6f4 v[224:227], v[148:155], v[74:81], v[38:41], v203, v202 op_sel_hi:[0,0,0]
	v_mfma_scale_f32_16x16x128_f8f6f4 v[228:231], v[140:147], v[82:89], v[30:33], v203, v202 op_sel_hi:[0,0,0]
	v_mfma_scale_f32_16x16x128_f8f6f4 v[232:235], v[148:155], v[82:89], v[22:25], v203, v202 op_sel_hi:[0,0,0]
	v_mfma_scale_f32_16x16x128_f8f6f4 v[236:239], v[140:147], v[90:97], v[14:17], v203, v202 op_sel_hi:[0,0,0]
	v_mfma_scale_f32_16x16x128_f8f6f4 v[240:243], v[148:155], v[90:97], v[6:9], v203, v202 op_sel_hi:[0,0,0]
	s_setprio 0
	s_setprio 1
	v_mfma_scale_f32_16x16x128_f8f6f4 v[58:61], v[170:177], v[66:73], v[58:61], v203, v202 op_sel_hi:[0,0,0]
	v_mfma_scale_f32_16x16x128_f8f6f4 v[50:53], v[178:185], v[66:73], v[50:53], v203, v202 op_sel_hi:[0,0,0]
	v_mfma_scale_f32_16x16x128_f8f6f4 v[42:45], v[170:177], v[74:81], v[42:45], v203, v202 op_sel_hi:[0,0,0]
	v_mfma_scale_f32_16x16x128_f8f6f4 v[244:247], v[178:185], v[74:81], v[34:37], v203, v202 op_sel_hi:[0,0,0]
	v_mfma_scale_f32_16x16x128_f8f6f4 v[198:201], v[170:177], v[82:89], v[26:29], v203, v202 op_sel_hi:[0,0,0]
	v_mfma_scale_f32_16x16x128_f8f6f4 v[134:137], v[178:185], v[82:89], v[18:21], v203, v202 op_sel_hi:[0,0,0]
	v_mfma_scale_f32_16x16x128_f8f6f4 v[66:69], v[170:177], v[90:97], v[10:13], v203, v202 op_sel_hi:[0,0,0]
	v_mfma_scale_f32_16x16x128_f8f6f4 v[74:77], v[178:185], v[90:97], v[2:5], v203, v202 op_sel_hi:[0,0,0]
	s_setprio 0
	s_barrier
; #define PG8_WAIT_V(n) asm volatile("s_waitcnt vmcnt(" #n ")" ::: "memory")
; #define PG8_WAIT_L(n) asm volatile("s_waitcnt lgkmcnt(" #n ")" ::: "memory")
; template <class Epi, class Sched, bool ALIGN_EPI = false, bool SP2 = false, bool FP8 = false>
; __device__ __forceinline__ void gemm_phase(PG8_LAS unsigned char* lds, const Gemm g, const Sched& S, const Epi& E, const int wave_) {
;     ...
;             PG8_WAIT_V(8); PG8_WAIT_L(0); PG8_BAR; PG8_MMA(1, 0, At, B0); PG8_MMA(1, 1, At, B1); PG8_BAR; PG8_SCHED;
;             PG8_LDB(B0, 1, 0); PG8_LDB(B1, 1, 1); PG8_SCHED; PG8_LDA(At, 1, 0); PG8_STAGE(PG8_SA(0, 1), a2 + hstep, voffA);
;             PG8_WAIT_V(8); PG8_WAIT_L(0); PG8_BAR; PG8_MMA(0, 0, At, B0); PG8_MMA(0, 1, At, B1); PG8_BAR; PG8_SCHED;
;             PG8_LDA(At, 1, 1); PG8_STAGE(PG8_SB(1, 0), b3, voffB); PG8_STAGE(PG8_SB(1, 1), b3 + hstep, voffB); PG8_STAGE(PG8_SA(1, 0), a3, voffA);
;             PG8_WAIT_V(8); PG8_WAIT_L(0); PG8_BAR; PG8_MMA(1, 0, At, B0); PG8_MMA(1, 1, At, B1); PG8_BAR; PG8_SCHED;
;             } else {
;             PG8_LDB(B0, 0, 0); PG8_SCHED; PG8_LDA(At, 0, 0); PG8_STAGE(PG8_SA(1, 1), a1 + hstep, voffA);
;             PG8_WAIT_L(8); PG8_BAR; PG8_WAIT_L(0); PG8_MMA(0, 0, At, B0); PG8_BAR; PG8_SCHED;
;             PG8_LDB(B1, 0, 1); PG8_STAGE(PG8_SB(0, 0), b2, voffB);
;             PG8_BAR; PG8_WAIT_L(0); PG8_MMA(0, 1, At, B1); PG8_BAR;
;             PG8_LDA(At, 0, 1); PG8_STAGE(PG8_SA(0, 0), a2, voffA);
;             PG8_BAR; PG8_WAIT_L(0); PG8_MMA(1, 0, At, B0); PG8_BAR; PG8_SCHED;
;             PG8_STAGE(PG8_SB(0, 1), b2 + hstep, voffB);
;             PG8_WAIT_V(6); PG8_BAR; PG8_MMA(1, 1, At, B1); PG8_BAR;
;             PG8_LDB(B0, 1, 0); PG8_SCHED; PG8_LDA(At, 1, 0); PG8_STAGE(PG8_SA(0, 1), a2 + hstep, voffA);
;             PG8_WAIT_L(8); PG8_BAR; PG8_WAIT_L(0); PG8_MMA(0, 0, At, B0); PG8_BAR; PG8_SCHED;
;             PG8_LDB(B1, 1, 1); PG8_STAGE(PG8_SB(1, 0), b3, voffB);
;             PG8_BAR; PG8_WAIT_L(0); PG8_MMA(0, 1, At, B1); PG8_BAR;
;             PG8_LDA(At, 1, 1); PG8_STAGE(PG8_SA(1, 0), a3, voffA);
;             PG8_BAR; PG8_WAIT_L(0); PG8_MMA(1, 0, At, B0); PG8_BAR; PG8_SCHED;
;             PG8_STAGE(PG8_SB(1, 1), b3 + hstep, voffB);
;             PG8_WAIT_V(6); PG8_BAR; PG8_MMA(1, 1, At, B1); PG8_BAR;
;             }
;         }
;         if constexpr (ALIGN_EPI) { if (wr == 0) PG8_BAR; }
	s_add_i32 s73, 0, 0x18000
	v_add_u32_e32 v0, s73, v138
	s_add_i32 s76, 0, 0x1c000
	s_nop 1
	ds_read_b128 v[2:5], v0
	ds_read_b128 v[6:9], v0 offset:1024
	ds_read_b128 v[140:143], v0 offset:2048
	ds_read_b128 v[144:147], v0 offset:3072
	v_add_u32_e32 v0, s76, v138
	ds_read_b128 v[148:151], v0
	ds_read_b128 v[152:155], v0 offset:1024
	ds_read_b128 v[170:173], v0 offset:2048
	ds_read_b128 v[174:177], v0 offset:3072
	s_add_u32 s74, s46, 0x40000
	v_mov_b32_e32 v0, v168
	s_mov_b32 m0, s61
	ds_read_b128 v[10:13], v139 offset:32768
	ds_read_b128 v[14:17], v139 offset:33792
	ds_read_b128 v[18:21], v139 offset:34816
	ds_read_b128 v[22:25], v139 offset:35840
	ds_read_b128 v[26:29], v139 offset:36864
	ds_read_b128 v[30:33], v139 offset:37888
	ds_read_b128 v[34:37], v139 offset:38912
	ds_read_b128 v[38:41], v139 offset:39936
	s_addc_u32 s75, s47, 0
	s_nop 0
	global_load_lds_dwordx4 v0, s[74:75]
	v_mov_b32_e32 v0, v248
	s_mov_b32 m0, s62
	s_nop 0
	global_load_lds_dwordx4 v0, s[74:75]
	s_waitcnt vmcnt(8)
	s_waitcnt lgkmcnt(0)
	s_barrier
	s_setprio 1
	s_waitcnt lgkmcnt(0)
	v_mfma_scale_f32_16x16x128_f8f6f4 v[126:129], v[2:9], v[10:17], v[126:129], v203, v202 op_sel_hi:[0,0,0]
	v_mfma_scale_f32_16x16x128_f8f6f4 v[118:121], v[140:147], v[10:17], v[118:121], v203, v202 op_sel_hi:[0,0,0]
	v_mfma_scale_f32_16x16x128_f8f6f4 v[110:113], v[2:9], v[18:25], v[110:113], v203, v202 op_sel_hi:[0,0,0]
	v_mfma_scale_f32_16x16x128_f8f6f4 v[102:105], v[140:147], v[18:25], v[102:105], v203, v202 op_sel_hi:[0,0,0]
	v_mfma_scale_f32_16x16x128_f8f6f4 v[94:97], v[2:9], v[26:33], v[130:133], v203, v202 op_sel_hi:[0,0,0]
	v_mfma_scale_f32_16x16x128_f8f6f4 v[86:89], v[140:147], v[26:33], v[156:159], v203, v202 op_sel_hi:[0,0,0]
	v_mfma_scale_f32_16x16x128_f8f6f4 v[78:81], v[2:9], v[34:41], v[160:163], v203, v202 op_sel_hi:[0,0,0]
	v_mfma_scale_f32_16x16x128_f8f6f4 v[70:73], v[140:147], v[34:41], v[164:167], v203, v202 op_sel_hi:[0,0,0]
	s_setprio 0
	s_setprio 1
	v_mfma_scale_f32_16x16x128_f8f6f4 v[122:125], v[148:155], v[10:17], v[122:125], v203, v202 op_sel_hi:[0,0,0]
	v_mfma_scale_f32_16x16x128_f8f6f4 v[114:117], v[170:177], v[10:17], v[114:117], v203, v202 op_sel_hi:[0,0,0]
	v_mfma_scale_f32_16x16x128_f8f6f4 v[106:109], v[148:155], v[18:25], v[106:109], v203, v202 op_sel_hi:[0,0,0]
	v_mfma_scale_f32_16x16x128_f8f6f4 v[98:101], v[170:177], v[18:25], v[98:101], v203, v202 op_sel_hi:[0,0,0]
	v_mfma_scale_f32_16x16x128_f8f6f4 v[90:93], v[148:155], v[26:33], v[186:189], v203, v202 op_sel_hi:[0,0,0]
	v_mfma_scale_f32_16x16x128_f8f6f4 v[82:85], v[170:177], v[26:33], v[190:193], v203, v202 op_sel_hi:[0,0,0]
	v_mfma_scale_f32_16x16x128_f8f6f4 v[194:197], v[148:155], v[34:41], v[194:197], v203, v202 op_sel_hi:[0,0,0]
	v_mfma_scale_f32_16x16x128_f8f6f4 v[204:207], v[170:177], v[34:41], v[204:207], v203, v202 op_sel_hi:[0,0,0]
	s_setprio 0
	s_barrier
	v_mov_b32_e32 v0, v169
	ds_read_b128 v[178:181], v139 offset:49152
	ds_read_b128 v[182:185], v139 offset:50176
	ds_read_b128 v[186:189], v139 offset:51200
	ds_read_b128 v[190:193], v139 offset:52224
	ds_read_b128 v[208:211], v139 offset:53248
	ds_read_b128 v[212:215], v139 offset:54272
	ds_read_b128 v[216:219], v139 offset:55296
	ds_read_b128 v[220:223], v139 offset:56320
	s_add_i32 s73, s73, s33
	s_add_u32 s98, s48, s6
	s_addc_u32 s99, s49, s7
	s_mov_b32 m0, s73
	v_mov_b32_e32 v0, v249
	global_load_lds_dwordx4 v169, s[98:99]
	s_add_i32 m0, s73, 0x2000
	s_nop 0
	s_add_u32 s98, s48, s6
	s_addc_u32 s99, s49, s7
	s_add_u32 s48, s48, 0x40080
	s_addc_u32 s49, s49, 0
	v_mov_b32_e32 v0, v169
	s_add_i32 s73, s76, s33
	global_load_lds_dwordx4 v249, s[98:99]
	s_mov_b32 m0, s73
	s_nop 0
	global_load_lds_dwordx4 v0, s[48:49]
	v_mov_b32_e32 v0, v249
	s_add_i32 m0, s73, 0x2000
	s_nop 0
	global_load_lds_dwordx4 v0, s[48:49]
	v_mov_b32_e32 v0, v168
	s_mov_b32 m0, s63
	s_add_u32 s98, s46, s6
	s_addc_u32 s99, s47, s7
	v_mov_b32_e32 v0, v248
	global_load_lds_dwordx4 v168, s[98:99]
	s_mov_b32 m0, s64
	s_add_u32 s98, s46, s6
	s_addc_u32 s99, s47, s7
	global_load_lds_dwordx4 v248, s[98:99]
	s_waitcnt vmcnt(8)
	s_waitcnt lgkmcnt(0)
	s_barrier
	s_setprio 1
	s_waitcnt lgkmcnt(0)
	v_mfma_scale_f32_16x16x128_f8f6f4 v[62:65], v[2:9], v[178:185], v[62:65], v203, v202 op_sel_hi:[0,0,0]
	v_mfma_scale_f32_16x16x128_f8f6f4 v[54:57], v[140:147], v[178:185], v[54:57], v203, v202 op_sel_hi:[0,0,0]
	v_mfma_scale_f32_16x16x128_f8f6f4 v[46:49], v[2:9], v[186:193], v[46:49], v203, v202 op_sel_hi:[0,0,0]
	v_mfma_scale_f32_16x16x128_f8f6f4 v[38:41], v[140:147], v[186:193], v[224:227], v203, v202 op_sel_hi:[0,0,0]
	v_mfma_scale_f32_16x16x128_f8f6f4 v[30:33], v[2:9], v[208:215], v[228:231], v203, v202 op_sel_hi:[0,0,0]
	v_mfma_scale_f32_16x16x128_f8f6f4 v[22:25], v[140:147], v[208:215], v[232:235], v203, v202 op_sel_hi:[0,0,0]
	v_mfma_scale_f32_16x16x128_f8f6f4 v[14:17], v[2:9], v[216:223], v[236:239], v203, v202 op_sel_hi:[0,0,0]
	v_mfma_scale_f32_16x16x128_f8f6f4 v[6:9], v[140:147], v[216:223], v[240:243], v203, v202 op_sel_hi:[0,0,0]
	s_setprio 0
	s_setprio 1
	v_mfma_scale_f32_16x16x128_f8f6f4 v[58:61], v[148:155], v[178:185], v[58:61], v203, v202 op_sel_hi:[0,0,0]
	v_mfma_scale_f32_16x16x128_f8f6f4 v[50:53], v[170:177], v[178:185], v[50:53], v203, v202 op_sel_hi:[0,0,0]
	v_mfma_scale_f32_16x16x128_f8f6f4 v[42:45], v[148:155], v[186:193], v[42:45], v203, v202 op_sel_hi:[0,0,0]
	v_mfma_scale_f32_16x16x128_f8f6f4 v[34:37], v[170:177], v[186:193], v[244:247], v203, v202 op_sel_hi:[0,0,0]
	v_mfma_scale_f32_16x16x128_f8f6f4 v[26:29], v[148:155], v[208:215], v[198:201], v203, v202 op_sel_hi:[0,0,0]
	v_mfma_scale_f32_16x16x128_f8f6f4 v[18:21], v[170:177], v[208:215], v[134:137], v203, v202 op_sel_hi:[0,0,0]
	v_mfma_scale_f32_16x16x128_f8f6f4 v[10:13], v[148:155], v[216:223], v[66:69], v203, v202 op_sel_hi:[0,0,0]
	v_mfma_scale_f32_16x16x128_f8f6f4 v[2:5], v[170:177], v[216:223], v[74:77], v203, v202 op_sel_hi:[0,0,0]
	s_setprio 0
	s_barrier
	s_add_i32 s72, s72, 2
	s_add_u32 s44, s44, 0x100
	s_addc_u32 s45, s45, 0
	s_add_u32 s70, s70, 0x100
	s_addc_u32 s71, s71, 0
	s_cmp_gt_u32 s72, 13
	s_cbranch_scc0 .LBB0_1849
	v_readlane_b32 s18, v252, 10
	v_readlane_b32 s19, v252, 11
	s_and_b64 vcc, exec, s[18:19]
	s_movk_i32 s70, 0x3000
	v_readlane_b32 s71, v254, 44
	s_cbranch_vccz .LBB0_1852
	s_barrier

; #define PG8_STAGE(bufoff, gbase, voff) do { _Pragma("unroll") for (int _i = 0; _i < 2; ++_i) { unsigned _vo = (voff)[_i]; asm volatile("" : "+v"(_vo));     \
;         __builtin_amdgcn_global_load_lds((const unsigned*)((const char*)(gbase) + _vo), (PG8_LAS unsigned*)(lds + (bufoff) + ldsw + _i * 8192), 16, 0, 0); } } while (0)
; #define PG8_LDA(dst, b, h) do { _Pragma("unroll") for (int m = 0; m < 4; ++m) _Pragma("unroll") for (int k = 0; k < 2; ++k) dst[m][k] = *(const PG8_LAS bf16x8*)(lds + PG8_SA(b, h) + aoff + m * 2048 + k * 1024); } while (0)
; #define PG8_LDB(dst, b, h) do { _Pragma("unroll") for (int n = 0; n < 2; ++n) _Pragma("unroll") for (int k = 0; k < 2; ++k) dst[n][k] = *(const PG8_LAS bf16x8*)(lds + PG8_SB(b, h) + boff + n * 2048 + k * 1024); } while (0)
; #define PG8_WAIT_V(n) asm volatile("s_waitcnt vmcnt(" #n ")" ::: "memory")
; #define PG8_WAIT_L(n) asm volatile("s_waitcnt lgkmcnt(" #n ")" ::: "memory")
; #define PG8_BAR __builtin_amdgcn_s_barrier()
; #define PG8_SCHED __builtin_amdgcn_sched_barrier(0)
; template <class Epi, class Sched, bool ALIGN_EPI = false, bool SP2 = false, bool FP8 = false>
; __device__ __forceinline__ void gemm_phase(PG8_LAS unsigned char* lds, const Gemm g, const Sched& S, const Epi& E, const int wave_) {
;     ...
;         for (int t = 0; t < ntc; t += 2) {
;             const bool last = (t == ntc - 2);
;             const char* a1 = cA + (size_t)(t + 1) * kstep;
;             const char* a2 = last ? nA : cA + (size_t)(t + 2) * kstep; const char* b2 = last ? nB : cB + (size_t)(t + 2) * kstep;
;             const char* a3 = a2 + kstep; const char* b3 = b2 + kstep;
;             if (last && has_next) S.a_ready(nxt);
;             if constexpr (SP2) {
;             PG8_LDB(B0, 0, 0); PG8_LDB(B1, 0, 1); PG8_SCHED; PG8_LDA(At, 0, 0); PG8_STAGE(PG8_SA(1, 1), a1 + hstep, voffA);
;             PG8_WAIT_V(8); PG8_WAIT_L(0); PG8_BAR; PG8_MMA(0, 0, At, B0); PG8_MMA(0, 1, At, B1); PG8_BAR; PG8_SCHED;
;             PG8_LDA(At, 0, 1); PG8_STAGE(PG8_SB(0, 0), b2, voffB); PG8_STAGE(PG8_SB(0, 1), b2 + hstep, voffB); PG8_STAGE(PG8_SA(0, 0), a2, voffA);
;             PG8_WAIT_V(8); PG8_WAIT_L(0); PG8_BAR; PG8_MMA(1, 0, At, B0); PG8_MMA(1, 1, At, B1); PG8_BAR; PG8_SCHED;
.LBB0_1954:
	s_add_i32 s81, s44, 2
	s_add_u32 s46, s42, 0xfff50080
	s_addc_u32 s45, s43, -1
	s_add_i32 s82, 0, 0x10000
	s_cmp_eq_u32 s19, s44
	s_cselect_b32 s45, s29, s45
	s_cselect_b32 s44, s28, s46
	v_add_u32_e32 v0, s82, v144
	s_cselect_b32 s47, s35, s80
	s_cselect_b32 s46, s34, s79
	s_add_i32 s84, 0, 0x14000
	ds_read_b128 v[130:133], v0
	ds_read_b128 v[134:137], v0 offset:1024
	ds_read_b128 v[146:149], v0 offset:2048
	ds_read_b128 v[150:153], v0 offset:3072
	v_add_u32_e32 v0, s84, v144
	ds_read_b128 v[154:157], v0
	ds_read_b128 v[158:161], v0 offset:1024
	ds_read_b128 v[170:173], v0 offset:2048
	ds_read_b128 v[174:177], v0 offset:3072
	v_mov_b32_e32 v0, v248
	ds_read_b128 v[178:181], v145
	ds_read_b128 v[182:185], v145 offset:1024
	ds_read_b128 v[186:189], v145 offset:2048
	ds_read_b128 v[190:193], v145 offset:3072
	ds_read_b128 v[208:211], v145 offset:4096
	ds_read_b128 v[212:215], v145 offset:5120
	ds_read_b128 v[216:219], v145 offset:6144
	ds_read_b128 v[220:223], v145 offset:7168
	s_add_i32 m0, s59, 0xc000
	s_nop 0
	global_load_lds_dwordx4 v0, s[42:43]
	v_mov_b32_e32 v0, v142
	s_add_i32 m0, s59, 0xe000
	s_nop 0
	global_load_lds_dwordx4 v0, s[42:43]
	s_waitcnt vmcnt(8)
	s_waitcnt lgkmcnt(0)
	s_barrier
	s_setprio 1
	s_waitcnt lgkmcnt(0)
	v_mfma_scale_f32_16x16x128_f8f6f4 v[126:129], v[130:137], v[178:185], v[126:129], v203, v202 op_sel_hi:[0,0,0]
	v_mfma_scale_f32_16x16x128_f8f6f4 v[122:125], v[146:153], v[178:185], v[122:125], v203, v202 op_sel_hi:[0,0,0]
	v_mfma_scale_f32_16x16x128_f8f6f4 v[110:113], v[130:137], v[186:193], v[110:113], v203, v202 op_sel_hi:[0,0,0]
	v_mfma_scale_f32_16x16x128_f8f6f4 v[106:109], v[146:153], v[186:193], v[106:109], v203, v202 op_sel_hi:[0,0,0]
	v_mfma_scale_f32_16x16x128_f8f6f4 v[162:165], v[130:137], v[208:215], v[94:97], v203, v202 op_sel_hi:[0,0,0]
	v_mfma_scale_f32_16x16x128_f8f6f4 v[166:169], v[146:153], v[208:215], v[90:93], v203, v202 op_sel_hi:[0,0,0]
	v_mfma_scale_f32_16x16x128_f8f6f4 v[194:197], v[130:137], v[216:223], v[78:81], v203, v202 op_sel_hi:[0,0,0]
	v_mfma_scale_f32_16x16x128_f8f6f4 v[198:201], v[146:153], v[216:223], v[74:77], v203, v202 op_sel_hi:[0,0,0]
	s_setprio 0
	s_setprio 1
	v_mfma_scale_f32_16x16x128_f8f6f4 v[118:121], v[154:161], v[178:185], v[118:121], v203, v202 op_sel_hi:[0,0,0]
	v_mfma_scale_f32_16x16x128_f8f6f4 v[114:117], v[170:177], v[178:185], v[114:117], v203, v202 op_sel_hi:[0,0,0]
	v_mfma_scale_f32_16x16x128_f8f6f4 v[102:105], v[154:161], v[186:193], v[102:105], v203, v202 op_sel_hi:[0,0,0]
	v_mfma_scale_f32_16x16x128_f8f6f4 v[98:101], v[170:177], v[186:193], v[98:101], v203, v202 op_sel_hi:[0,0,0]
	v_mfma_scale_f32_16x16x128_f8f6f4 v[178:181], v[154:161], v[208:215], v[86:89], v203, v202 op_sel_hi:[0,0,0]
	v_mfma_scale_f32_16x16x128_f8f6f4 v[182:185], v[170:177], v[208:215], v[82:85], v203, v202 op_sel_hi:[0,0,0]
	v_mfma_scale_f32_16x16x128_f8f6f4 v[186:189], v[154:161], v[216:223], v[70:73], v203, v202 op_sel_hi:[0,0,0]
	v_mfma_scale_f32_16x16x128_f8f6f4 v[190:193], v[170:177], v[216:223], v[66:69], v203, v202 op_sel_hi:[0,0,0]
	s_setprio 0
	s_barrier
	v_mov_b32_e32 v0, v249
	s_add_i32 s82, s82, s33
	s_nop 2
	ds_read_b128 v[66:69], v145 offset:16384
	ds_read_b128 v[70:73], v145 offset:17408
	ds_read_b128 v[74:77], v145 offset:18432
	ds_read_b128 v[78:81], v145 offset:19456
	ds_read_b128 v[82:85], v145 offset:20480
	ds_read_b128 v[86:89], v145 offset:21504
	ds_read_b128 v[90:93], v145 offset:22528
	ds_read_b128 v[94:97], v145 offset:23552
	s_mov_b32 m0, s82
	s_nop 0
	global_load_lds_dwordx4 v0, s[46:47]
	v_mov_b32_e32 v0, v143
	s_add_i32 m0, s82, 0x2000
	s_add_u32 s82, s46, 0xb0000
	global_load_lds_dwordx4 v0, s[46:47]
	s_addc_u32 s83, s47, 0
	v_mov_b32_e32 v0, v249
	s_add_i32 s84, s84, s33
	s_mov_b32 m0, s84
	s_nop 0
	global_load_lds_dwordx4 v0, s[82:83]
	v_mov_b32_e32 v0, v143
	s_add_i32 m0, s84, 0x2000
	s_nop 0
	global_load_lds_dwordx4 v0, s[82:83]
	v_mov_b32_e32 v0, v248
	s_mov_b32 m0, s59
	s_nop 0
	global_load_lds_dwordx4 v0, s[44:45]
	v_mov_b32_e32 v0, v142
	s_mov_b32 m0, s60
	s_nop 0
	global_load_lds_dwordx4 v0, s[44:45]
	s_waitcnt vmcnt(8)
	s_waitcnt lgkmcnt(0)
	s_barrier
	s_setprio 1
	s_waitcnt lgkmcnt(0)
	v_mfma_scale_f32_16x16x128_f8f6f4 v[62:65], v[130:137], v[66:73], v[62:65], v203, v202 op_sel_hi:[0,0,0]
	v_mfma_scale_f32_16x16x128_f8f6f4 v[58:61], v[146:153], v[66:73], v[58:61], v203, v202 op_sel_hi:[0,0,0]
	v_mfma_scale_f32_16x16x128_f8f6f4 v[204:207], v[130:137], v[74:81], v[46:49], v203, v202 op_sel_hi:[0,0,0]
	v_mfma_scale_f32_16x16x128_f8f6f4 v[208:211], v[146:153], v[74:81], v[42:45], v203, v202 op_sel_hi:[0,0,0]
	v_mfma_scale_f32_16x16x128_f8f6f4 v[212:215], v[130:137], v[82:89], v[30:33], v203, v202 op_sel_hi:[0,0,0]
	v_mfma_scale_f32_16x16x128_f8f6f4 v[216:219], v[146:153], v[82:89], v[26:29], v203, v202 op_sel_hi:[0,0,0]
	v_mfma_scale_f32_16x16x128_f8f6f4 v[220:223], v[130:137], v[90:97], v[14:17], v203, v202 op_sel_hi:[0,0,0]
	v_mfma_scale_f32_16x16x128_f8f6f4 v[224:227], v[146:153], v[90:97], v[10:13], v203, v202 op_sel_hi:[0,0,0]
	s_setprio 0
	s_setprio 1
	v_mfma_scale_f32_16x16x128_f8f6f4 v[54:57], v[154:161], v[66:73], v[54:57], v203, v202 op_sel_hi:[0,0,0]
	v_mfma_scale_f32_16x16x128_f8f6f4 v[50:53], v[170:177], v[66:73], v[50:53], v203, v202 op_sel_hi:[0,0,0]
	v_mfma_scale_f32_16x16x128_f8f6f4 v[228:231], v[154:161], v[74:81], v[38:41], v203, v202 op_sel_hi:[0,0,0]
	v_mfma_scale_f32_16x16x128_f8f6f4 v[232:235], v[170:177], v[74:81], v[34:37], v203, v202 op_sel_hi:[0,0,0]
	v_mfma_scale_f32_16x16x128_f8f6f4 v[236:239], v[154:161], v[82:89], v[22:25], v203, v202 op_sel_hi:[0,0,0]
	v_mfma_scale_f32_16x16x128_f8f6f4 v[240:243], v[170:177], v[82:89], v[18:21], v203, v202 op_sel_hi:[0,0,0]
	v_mfma_scale_f32_16x16x128_f8f6f4 v[244:247], v[154:161], v[90:97], v[6:9], v203, v202 op_sel_hi:[0,0,0]
	v_mfma_scale_f32_16x16x128_f8f6f4 v[138:141], v[170:177], v[90:97], v[2:5], v203, v202 op_sel_hi:[0,0,0]
	s_setprio 0
	s_barrier
; #define PG8_STAGE(bufoff, gbase, voff) do { _Pragma("unroll") for (int _i = 0; _i < 2; ++_i) { unsigned _vo = (voff)[_i]; asm volatile("" : "+v"(_vo));     \
;         __builtin_amdgcn_global_load_lds((const unsigned*)((const char*)(gbase) + _vo), (PG8_LAS unsigned*)(lds + (bufoff) + ldsw + _i * 8192), 16, 0, 0); } } while (0)
; #define PG8_LDA(dst, b, h) do { _Pragma("unroll") for (int m = 0; m < 4; ++m) _Pragma("unroll") for (int k = 0; k < 2; ++k) dst[m][k] = *(const PG8_LAS bf16x8*)(lds + PG8_SA(b, h) + aoff + m * 2048 + k * 1024); } while (0)
; #define PG8_LDB(dst, b, h) do { _Pragma("unroll") for (int n = 0; n < 2; ++n) _Pragma("unroll") for (int k = 0; k < 2; ++k) dst[n][k] = *(const PG8_LAS bf16x8*)(lds + PG8_SB(b, h) + boff + n * 2048 + k * 1024); } while (0)
; #define PG8_WAIT_V(n) asm volatile("s_waitcnt vmcnt(" #n ")" ::: "memory")
; #define PG8_WAIT_L(n) asm volatile("s_waitcnt lgkmcnt(" #n ")" ::: "memory")
; #define PG8_BAR __builtin_amdgcn_s_barrier()
; #define PG8_SCHED __builtin_amdgcn_sched_barrier(0)
; template <class Epi, class Sched, bool ALIGN_EPI = false, bool SP2 = false, bool FP8 = false>
; __device__ __forceinline__ void gemm_phase(PG8_LAS unsigned char* lds, const Gemm g, const Sched& S, const Epi& E, const int wave_) {
;     ...
;             PG8_LDB(B0, 1, 0); PG8_LDB(B1, 1, 1); PG8_SCHED; PG8_LDA(At, 1, 0); PG8_STAGE(PG8_SA(0, 1), a2 + hstep, voffA);
;             PG8_WAIT_V(8); PG8_WAIT_L(0); PG8_BAR; PG8_MMA(0, 0, At, B0); PG8_MMA(0, 1, At, B1); PG8_BAR; PG8_SCHED;
;             PG8_LDA(At, 1, 1); PG8_STAGE(PG8_SB(1, 0), b3, voffB); PG8_STAGE(PG8_SB(1, 1), b3 + hstep, voffB); PG8_STAGE(PG8_SA(1, 0), a3, voffA);
;             PG8_WAIT_V(8); PG8_WAIT_L(0); PG8_BAR; PG8_MMA(1, 0, At, B0); PG8_MMA(1, 1, At, B1); PG8_BAR; PG8_SCHED;
	s_add_i32 s84, 0, 0x18000
	v_add_u32_e32 v0, s84, v144
	s_add_i32 s85, 0, 0x1c000
	s_nop 1
	ds_read_b128 v[2:5], v0
	ds_read_b128 v[6:9], v0 offset:1024
	ds_read_b128 v[18:21], v0 offset:2048
	ds_read_b128 v[22:25], v0 offset:3072
	v_add_u32_e32 v0, s85, v144
	ds_read_b128 v[130:133], v0
	ds_read_b128 v[134:137], v0 offset:1024
	ds_read_b128 v[146:149], v0 offset:2048
	ds_read_b128 v[150:153], v0 offset:3072
	s_add_u32 s82, s44, 0xb0000
	v_mov_b32_e32 v0, v248
	s_mov_b32 m0, s61
	ds_read_b128 v[10:13], v145 offset:32768
	ds_read_b128 v[14:17], v145 offset:33792
	ds_read_b128 v[26:29], v145 offset:34816
	ds_read_b128 v[30:33], v145 offset:35840
	ds_read_b128 v[34:37], v145 offset:36864
	ds_read_b128 v[38:41], v145 offset:37888
	ds_read_b128 v[42:45], v145 offset:38912
	ds_read_b128 v[46:49], v145 offset:39936
	s_addc_u32 s83, s45, 0
	s_nop 0
	global_load_lds_dwordx4 v0, s[82:83]
	v_mov_b32_e32 v0, v142
	s_mov_b32 m0, s62
	s_nop 0
	global_load_lds_dwordx4 v0, s[82:83]
	s_waitcnt vmcnt(8)
	s_waitcnt lgkmcnt(0)
	s_barrier
	s_setprio 1
	s_waitcnt lgkmcnt(0)
	v_mfma_scale_f32_16x16x128_f8f6f4 v[126:129], v[2:9], v[10:17], v[126:129], v203, v202 op_sel_hi:[0,0,0]
	v_mfma_scale_f32_16x16x128_f8f6f4 v[122:125], v[18:25], v[10:17], v[122:125], v203, v202 op_sel_hi:[0,0,0]
	v_mfma_scale_f32_16x16x128_f8f6f4 v[110:113], v[2:9], v[26:33], v[110:113], v203, v202 op_sel_hi:[0,0,0]
	v_mfma_scale_f32_16x16x128_f8f6f4 v[106:109], v[18:25], v[26:33], v[106:109], v203, v202 op_sel_hi:[0,0,0]
	v_mfma_scale_f32_16x16x128_f8f6f4 v[94:97], v[2:9], v[34:41], v[162:165], v203, v202 op_sel_hi:[0,0,0]
	v_mfma_scale_f32_16x16x128_f8f6f4 v[90:93], v[18:25], v[34:41], v[166:169], v203, v202 op_sel_hi:[0,0,0]
	v_mfma_scale_f32_16x16x128_f8f6f4 v[78:81], v[2:9], v[42:49], v[194:197], v203, v202 op_sel_hi:[0,0,0]
	v_mfma_scale_f32_16x16x128_f8f6f4 v[74:77], v[18:25], v[42:49], v[198:201], v203, v202 op_sel_hi:[0,0,0]
	s_setprio 0
	s_setprio 1
	v_mfma_scale_f32_16x16x128_f8f6f4 v[118:121], v[130:137], v[10:17], v[118:121], v203, v202 op_sel_hi:[0,0,0]
	v_mfma_scale_f32_16x16x128_f8f6f4 v[114:117], v[146:153], v[10:17], v[114:117], v203, v202 op_sel_hi:[0,0,0]
	v_mfma_scale_f32_16x16x128_f8f6f4 v[102:105], v[130:137], v[26:33], v[102:105], v203, v202 op_sel_hi:[0,0,0]
	v_mfma_scale_f32_16x16x128_f8f6f4 v[98:101], v[146:153], v[26:33], v[98:101], v203, v202 op_sel_hi:[0,0,0]
	v_mfma_scale_f32_16x16x128_f8f6f4 v[86:89], v[130:137], v[34:41], v[178:181], v203, v202 op_sel_hi:[0,0,0]
	v_mfma_scale_f32_16x16x128_f8f6f4 v[82:85], v[146:153], v[34:41], v[182:185], v203, v202 op_sel_hi:[0,0,0]
	v_mfma_scale_f32_16x16x128_f8f6f4 v[70:73], v[130:137], v[42:49], v[186:189], v203, v202 op_sel_hi:[0,0,0]
	v_mfma_scale_f32_16x16x128_f8f6f4 v[66:69], v[146:153], v[42:49], v[190:193], v203, v202 op_sel_hi:[0,0,0]
	s_setprio 0
	s_barrier
	v_mov_b32_e32 v0, v249
	ds_read_b128 v[34:37], v145 offset:49152
	ds_read_b128 v[38:41], v145 offset:50176
	ds_read_b128 v[154:157], v145 offset:51200
	ds_read_b128 v[158:161], v145 offset:52224
	ds_read_b128 v[170:173], v145 offset:53248
	ds_read_b128 v[174:177], v145 offset:54272
	ds_read_b128 v[178:181], v145 offset:55296
	ds_read_b128 v[182:185], v145 offset:56320
	s_add_i32 s82, s84, s33
	s_add_u32 s98, s46, s6
	s_addc_u32 s99, s47, s7
	s_mov_b32 m0, s82
	v_mov_b32_e32 v0, v143
	global_load_lds_dwordx4 v249, s[98:99]
	s_add_i32 m0, s82, 0x2000
	s_nop 0
	s_add_u32 s98, s46, s6
	s_addc_u32 s99, s47, s7
	s_add_u32 s46, s46, 0xb0080
	s_addc_u32 s47, s47, 0
	v_mov_b32_e32 v0, v249
	s_add_i32 s82, s85, s33
	global_load_lds_dwordx4 v143, s[98:99]
	s_mov_b32 m0, s82
	s_nop 0
	global_load_lds_dwordx4 v0, s[46:47]
	v_mov_b32_e32 v0, v143
	s_add_i32 m0, s82, 0x2000
	s_nop 0
	global_load_lds_dwordx4 v0, s[46:47]
	v_mov_b32_e32 v0, v248
	s_mov_b32 m0, s69
	s_add_u32 s98, s44, s6
	s_addc_u32 s99, s45, s7
	v_mov_b32_e32 v0, v142
	global_load_lds_dwordx4 v248, s[98:99]
	s_mov_b32 m0, s70
	s_add_u32 s98, s44, s6
	s_addc_u32 s99, s45, s7
	global_load_lds_dwordx4 v142, s[98:99]
	s_waitcnt vmcnt(8)
	s_waitcnt lgkmcnt(0)
	s_barrier
	s_setprio 1
	s_waitcnt lgkmcnt(0)
	v_mfma_scale_f32_16x16x128_f8f6f4 v[62:65], v[2:9], v[34:41], v[62:65], v203, v202 op_sel_hi:[0,0,0]
	v_mfma_scale_f32_16x16x128_f8f6f4 v[58:61], v[18:25], v[34:41], v[58:61], v203, v202 op_sel_hi:[0,0,0]
	v_mfma_scale_f32_16x16x128_f8f6f4 v[46:49], v[2:9], v[154:161], v[204:207], v203, v202 op_sel_hi:[0,0,0]
	v_mfma_scale_f32_16x16x128_f8f6f4 v[42:45], v[18:25], v[154:161], v[208:211], v203, v202 op_sel_hi:[0,0,0]
	v_mfma_scale_f32_16x16x128_f8f6f4 v[30:33], v[2:9], v[170:177], v[212:215], v203, v202 op_sel_hi:[0,0,0]
	v_mfma_scale_f32_16x16x128_f8f6f4 v[26:29], v[18:25], v[170:177], v[216:219], v203, v202 op_sel_hi:[0,0,0]
	v_mfma_scale_f32_16x16x128_f8f6f4 v[14:17], v[2:9], v[178:185], v[220:223], v203, v202 op_sel_hi:[0,0,0]
	v_mfma_scale_f32_16x16x128_f8f6f4 v[10:13], v[18:25], v[178:185], v[224:227], v203, v202 op_sel_hi:[0,0,0]
	s_setprio 0
	s_setprio 1
	v_mfma_scale_f32_16x16x128_f8f6f4 v[54:57], v[130:137], v[34:41], v[54:57], v203, v202 op_sel_hi:[0,0,0]
	v_mfma_scale_f32_16x16x128_f8f6f4 v[50:53], v[146:153], v[34:41], v[50:53], v203, v202 op_sel_hi:[0,0,0]
	v_mfma_scale_f32_16x16x128_f8f6f4 v[38:41], v[130:137], v[154:161], v[228:231], v203, v202 op_sel_hi:[0,0,0]
	v_mfma_scale_f32_16x16x128_f8f6f4 v[34:37], v[146:153], v[154:161], v[232:235], v203, v202 op_sel_hi:[0,0,0]
	v_mfma_scale_f32_16x16x128_f8f6f4 v[22:25], v[130:137], v[170:177], v[236:239], v203, v202 op_sel_hi:[0,0,0]
	v_mfma_scale_f32_16x16x128_f8f6f4 v[18:21], v[146:153], v[170:177], v[240:243], v203, v202 op_sel_hi:[0,0,0]
	v_mfma_scale_f32_16x16x128_f8f6f4 v[6:9], v[130:137], v[178:185], v[244:247], v203, v202 op_sel_hi:[0,0,0]
	v_mfma_scale_f32_16x16x128_f8f6f4 v[2:5], v[146:153], v[178:185], v[138:141], v203, v202 op_sel_hi:[0,0,0]
	s_setprio 0
	s_barrier
	s_add_u32 s42, s42, 0x100
	s_addc_u32 s43, s43, 0
	s_add_u32 s79, s79, 0x100
	s_addc_u32 s80, s80, 0
	s_cmp_ge_i32 s81, s18
	s_mov_b32 s44, s81
	s_cbranch_scc0 .LBB0_1954
	v_mov_b32_e32 v204, v250
	v_mov_b32_e32 v205, 0x260
	v_mov_b32_e32 v206, 0xff800000
	s_branch .LBB0_1959
